# retention state update (forward sweep + chunk loop): B-fragment LDS reads rotate through four register quads issued three MFMAs ahead with counted waits instead of one quad drained before every MFMA
# speedup vs baseline: 1.0225x; 1.0225x over previous
; #define LAS __attribute__((address_space(3)))
; __device__ __forceinline__ bf16x8 pack8(const float (&f)[8]) { u32x4 u; u.x = cvtpk(f[0], f[1]); u.y = cvtpk(f[2], f[3]); u.z = cvtpk(f[4], f[5]); u.w = cvtpk(f[6], f[7]); return __builtin_bit_cast(bf16x8, u); }
; __device__ __forceinline__ void kv_store(LAS unsigned char* lds, const KVRaw& R, int tid) {
; #pragma unroll
;     for (int i = 0; i < 2; ++i) {
;         const int q2 = tid + 512 * i, row = q2 >> 3, pc = q2 & 7;
;         float fa[8], fb[8], o1[8], o2[8];
;         unpack8(R.ka[i], fa); unpack8(R.kb[i], fb);
;         const float cs[8] = {R.c0[i].x, R.c0[i].y, R.c0[i].z, R.c0[i].w, R.c1[i].x, R.c1[i].y, R.c1[i].z, R.c1[i].w}, sn[8] = {R.s0[i].x, R.s0[i].y, R.s0[i].z, R.s0[i].w, R.s1[i].x, R.s1[i].y, R.s1[i].z, R.s1[i].w};
; #pragma unroll
;         for (int e = 0; e < 8; ++e) { o1[e] = fa[e] * cs[e] - fb[e] * sn[e]; o2[e] = fb[e] * cs[e] + fa[e] * sn[e]; }
;         *(LAS bf16x8*)(lds + LK + offb(row, pc)) = pack8(o1); *(LAS bf16x8*)(lds + LK + offb(row, pc + 8)) = pack8(o2);
;     }
; #pragma unroll
;     for (int i = 0; i < 4; ++i) { const int q4 = tid + 512 * i, row = q4 >> 4, ch = q4 & 15; *(LAS bf16x8*)(lds + LV + offb(row, ch)) = R.v[i]; }
; }
; __device__ __forceinline__ void unit(const bf16_t* __restrict__ proj, const float* __restrict__ rope, const float* __restrict__ log_decay, const float* __restrict__ gn_g, bf16_t* __restrict__ ymix, ...
;     ...
;     for (int n = 0; n < n0; ++n) {
;         RET_LANE
;         float lf2 = lf2_; asm volatile("" : "+v"(lf2));
;         __syncthreads();
;         kv_store(lds, raw, tid);
;         __syncthreads();
;         kv_load(raw, proj, rope, b, h, n + 1, tid);
.LBB0_287:
	s_waitcnt vmcnt(15)
	v_lshlrev_b32_e32 v100, 16, v76
	v_and_b32_e32 v101, 0xffff0000, v76
	s_waitcnt vmcnt(14)
	v_lshlrev_b32_e32 v102, 16, v72
	v_and_b32_e32 v103, 0xffff0000, v72
	s_waitcnt vmcnt(10)
	v_pk_mul_f32 v[104:105], v[92:93], v[100:101]
	v_pk_mul_f32 v[92:93], v[92:93], v[102:103]
	v_lshlrev_b32_e32 v76, 16, v77
	v_and_b32_e32 v77, 0xffff0000, v77
	v_pk_fma_f32 v[104:105], v[88:89], v[102:103], v[104:105]
	v_pk_fma_f32 v[88:89], v[88:89], v[100:101], v[92:93] neg_lo:[0,0,1] neg_hi:[0,0,1]
	v_lshlrev_b32_e32 v72, 16, v73
	v_and_b32_e32 v73, 0xffff0000, v73
	v_pk_mul_f32 v[92:93], v[94:95], v[76:77]
	v_mov_b32_e32 v98, v201
	v_pk_fma_f32 v[92:93], v[90:91], v[72:73], v[92:93]
	v_pk_mul_f32 v[72:73], v[94:95], v[72:73]
	v_mov_b32_e32 v115, v203
	v_pk_fma_f32 v[76:77], v[90:91], v[76:77], v[72:73] neg_lo:[0,0,1] neg_hi:[0,0,1]
	v_lshlrev_b32_e32 v72, 16, v78
	v_and_b32_e32 v73, 0xffff0000, v78
	v_lshlrev_b32_e32 v90, 16, v74
	v_and_b32_e32 v91, 0xffff0000, v74
	v_pk_mul_f32 v[94:95], v[84:85], v[72:73]
	v_pk_mul_f32 v[84:85], v[84:85], v[90:91]
	v_pk_fma_f32 v[94:95], v[80:81], v[90:91], v[94:95]
	v_pk_fma_f32 v[80:81], v[80:81], v[72:73], v[84:85] neg_lo:[0,0,1] neg_hi:[0,0,1]
	v_lshlrev_b32_e32 v72, 16, v79
	v_and_b32_e32 v73, 0xffff0000, v79
	v_lshlrev_b32_e32 v97, 4, v98
	v_lshlrev_b32_e32 v74, 16, v75
	v_and_b32_e32 v75, 0xffff0000, v75
	v_pk_mul_f32 v[78:79], v[86:87], v[72:73]
	v_and_b32_e32 v96, 0x70, v97
	v_pk_fma_f32 v[78:79], v[82:83], v[74:75], v[78:79]
	v_pk_mul_f32 v[74:75], v[86:87], v[74:75]
	v_add_u32_e32 v96, 0, v96
	v_pk_fma_f32 v[82:83], v[82:83], v[72:73], v[74:75] neg_lo:[0,0,1] neg_hi:[0,0,1]
	v_ashrrev_i32_e32 v84, 3, v98
	v_cvt_pk_bf16_f32 v72, v88, v89
	v_cvt_pk_bf16_f32 v73, v76, v77
	v_cvt_pk_bf16_f32 v74, v80, v81
	v_cvt_pk_bf16_f32 v75, v82, v83
	v_mad_u64_u32 v[76:77], s[38:39], v84, s68, v[96:97]
	s_barrier
	ds_write_b128 v76, v[72:75]
	v_cvt_pk_bf16_f32 v72, v104, v105
	v_cvt_pk_bf16_f32 v73, v92, v93
	v_cvt_pk_bf16_f32 v74, v94, v95
	v_cvt_pk_bf16_f32 v75, v78, v79
	ds_write_b128 v76, v[72:75] offset:128
	s_waitcnt vmcnt(9)
	v_lshlrev_b32_e32 v72, 16, v44
	v_and_b32_e32 v73, 0xffff0000, v44
	s_waitcnt vmcnt(8)
	v_lshlrev_b32_e32 v74, 16, v40
	v_and_b32_e32 v75, 0xffff0000, v40
	s_waitcnt vmcnt(4)
	v_pk_mul_f32 v[76:77], v[68:69], v[72:73]
	v_pk_mul_f32 v[68:69], v[68:69], v[74:75]
	v_lshlrev_b32_e32 v44, 16, v45
	v_and_b32_e32 v45, 0xffff0000, v45
	v_pk_fma_f32 v[76:77], v[64:65], v[74:75], v[76:77]
	v_pk_fma_f32 v[64:65], v[64:65], v[72:73], v[68:69] neg_lo:[0,0,1] neg_hi:[0,0,1]
	v_lshlrev_b32_e32 v40, 16, v41
	v_and_b32_e32 v41, 0xffff0000, v41
	v_pk_mul_f32 v[68:69], v[70:71], v[44:45]
	v_add_u32_e32 v78, 0x200, v98
	v_pk_fma_f32 v[68:69], v[66:67], v[40:41], v[68:69]
	v_pk_mul_f32 v[40:41], v[70:71], v[40:41]
	v_ashrrev_i32_e32 v99, 4, v78
	v_pk_fma_f32 v[40:41], v[66:67], v[44:45], v[40:41] neg_lo:[0,0,1] neg_hi:[0,0,1]
	v_lshlrev_b32_e32 v44, 16, v46
	v_and_b32_e32 v45, 0xffff0000, v46
	v_lshlrev_b32_e32 v66, 16, v42
	v_and_b32_e32 v67, 0xffff0000, v42
	v_pk_mul_f32 v[70:71], v[36:37], v[44:45]
	v_pk_mul_f32 v[36:37], v[36:37], v[66:67]
	v_pk_fma_f32 v[70:71], v[32:33], v[66:67], v[70:71]
	v_pk_fma_f32 v[36:37], v[32:33], v[44:45], v[36:37] neg_lo:[0,0,1] neg_hi:[0,0,1]
	v_lshlrev_b32_e32 v32, 16, v47
	v_and_b32_e32 v33, 0xffff0000, v47
	v_lshlrev_b32_e32 v42, 16, v43
	v_and_b32_e32 v43, 0xffff0000, v43
	v_pk_mul_f32 v[44:45], v[38:39], v[32:33]
	v_pk_mul_f32 v[38:39], v[38:39], v[42:43]
	v_pk_fma_f32 v[44:45], v[34:35], v[42:43], v[44:45]
	v_pk_fma_f32 v[38:39], v[34:35], v[32:33], v[38:39] neg_lo:[0,0,1] neg_hi:[0,0,1]
	v_ashrrev_i32_e32 v42, 3, v78
	v_cvt_pk_bf16_f32 v32, v64, v65
	v_cvt_pk_bf16_f32 v33, v40, v41
	v_cvt_pk_bf16_f32 v34, v36, v37
	v_cvt_pk_bf16_f32 v35, v38, v39
	v_mad_u64_u32 v[36:37], s[38:39], v42, s68, v[96:97]
	ds_write_b128 v36, v[32:35]
	v_cvt_pk_bf16_f32 v32, v76, v77
	v_cvt_pk_bf16_f32 v33, v68, v69
	v_cvt_pk_bf16_f32 v34, v70, v71
	v_cvt_pk_bf16_f32 v35, v44, v45
	v_and_b32_e32 v96, 0xf0, v97
	ds_write_b128 v36, v[32:35] offset:128
	v_add_u32_e32 v32, 0, v96
	v_ashrrev_i32_e32 v97, 4, v98
	v_mad_u64_u32 v[34:35], s[38:39], v97, s68, v[32:33]
	s_waitcnt vmcnt(2)
	ds_write_b128 v34, v[48:51] offset:36864
	v_mad_u64_u32 v[34:35], s[38:39], v99, s68, v[32:33]
	v_add_u32_e32 v33, 0x400, v98
	v_ashrrev_i32_e32 v100, 4, v33
	s_waitcnt vmcnt(1)
	ds_write_b128 v34, v[52:55] offset:36864
	v_mad_u64_u32 v[34:35], s[38:39], v100, s68, v[32:33]
	v_add_u32_e32 v33, 0x600, v98
	v_ashrrev_i32_e32 v101, 4, v33
	v_mad_u64_u32 v[32:33], s[38:39], v101, s68, v[32:33]
	v_lshlrev_b32_e32 v102, 3, v98
	s_add_i32 s9, s3, s4
	ds_write_b128 v34, v[60:63] offset:36864
	s_waitcnt vmcnt(0)
	ds_write_b128 v32, v[56:59] offset:36864
	v_and_b32_e32 v38, 56, v102
	v_add_u32_e32 v34, s9, v84
	v_mov_b64_e32 v[56:57], s[30:31]
	v_lshlrev_b32_e32 v176, 2, v38
	v_mad_i64_i32 v[34:35], s[38:39], v34, s67, v[56:57]
	v_lshl_add_u64 v[32:33], s[20:21], 0, v[176:177]
	v_lshl_add_u64 v[36:37], s[14:15], 0, v[176:177]
	v_lshl_add_u64 v[34:35], v[34:35], 0, v[180:181]
	v_lshlrev_b32_e32 v176, 1, v38
	v_lshl_add_u64 v[34:35], v[34:35], 0, v[176:177]
	v_lshl_add_u64 v[38:39], v[34:35], 0, s[22:23]
	v_add_co_u32_e32 v34, vcc, s69, v34
	v_add_u32_e32 v40, s4, v84
	s_nop 0
	v_addc_co_u32_e32 v35, vcc, 0, v35, vcc
	s_waitcnt lgkmcnt(0)
	s_barrier
; __device__ __forceinline__ bf16x8 pack8(const float (&f)[8]) { u32x4 u; u.x = cvtpk(f[0], f[1]); u.y = cvtpk(f[2], f[3]); u.z = cvtpk(f[4], f[5]); u.w = cvtpk(f[6], f[7]); return __builtin_bit_cast(bf16x8, u); }
; __device__ __forceinline__ void kv_load(KVRaw& R, const bf16_t* __restrict__ proj, const float* __restrict__ rope, int b, int h, int n, int tid) {
; #pragma unroll
;     for (int i = 0; i < 2; ++i) {
;         const int q2 = tid + 512 * i, row = q2 >> 3, pc = q2 & 7, t = n * 128 + row;
;         const bf16_t* rp = proj + (size_t)(b * SEQ + t) * DIN + OFF_KR + h * 128;
;         R.ka[i] = *(const bf16x8*)(rp + pc * 8); R.kb[i] = *(const bf16x8*)(rp + 64 + pc * 8);
;         R.c0[i] = *(const f32x4*)(rope + t * 64 + pc * 8); R.c1[i] = *(const f32x4*)(rope + t * 64 + pc * 8 + 4);
;         R.s0[i] = *(const f32x4*)(rope + SEQ * 64 + t * 64 + pc * 8); R.s1[i] = *(const f32x4*)(rope + SEQ * 64 + t * 64 + pc * 8 + 4);
;     }
; #pragma unroll
;     for (int i = 0; i < 4; ++i) { const int q4 = tid + 512 * i, row = q4 >> 4, ch = q4 & 15, t = n * 128 + row;
;         R.v[i] = *(const bf16x8*)(proj + (size_t)(b * SEQ + t) * DIN + OFF_VR + h * 128 + ch * 8); }
; }
; template <bool FWD> __device__ __forceinline__ void state_update_1(LAS unsigned char* lds, f32x4 (&racc)[8], float l2, int w, int g, unsigned qp, unsigned p) {
;     const float dec = __builtin_amdgcn_exp2f(128.f * l2);
;     bf16x8 vs[4];
; #pragma unroll
;     for (int ks = 0; ks < 4; ++ks) {
;         float f[8]; unpack8(trfrag(lds + LV, 32 * ks + 4 * g, 32 * ks + 16 + 4 * g, w, qp, p), f);
; #pragma unroll
;         for (int e = 0; e < 8; ++e) { const int key = 32 * ks + 16 * (e >> 2) + 4 * g + (e & 3); f[e] *= __builtin_amdgcn_exp2f((FWD ? (float)(127 - key) : (float)key) * l2); }
;         vs[ks] = pack8(f);
;     }
	global_load_dwordx4 v[76:79], v[34:35], off
	global_load_dwordx4 v[72:75], v[38:39], off offset:128
	v_lshl_add_u32 v34, v40, 6, v199
	v_ashrrev_i32_e32 v35, 31, v34
	v_lshlrev_b64 v[34:35], 2, v[34:35]
	v_lshl_add_u64 v[38:39], v[32:33], 0, v[34:35]
	v_lshl_add_u64 v[34:35], v[36:37], 0, v[34:35]
	global_load_dwordx4 v[80:83], v[38:39], off offset:16
	global_load_dwordx4 v[88:91], v[38:39], off
	global_load_dwordx4 v[84:87], v[34:35], off offset:16
	global_load_dwordx4 v[92:95], v[34:35], off
	v_add_u32_e32 v34, s9, v42
	v_mad_i64_i32 v[34:35], s[38:39], v34, s67, v[56:57]
	v_lshl_add_u64 v[34:35], v[34:35], 0, v[180:181]
	v_lshl_add_u64 v[34:35], v[34:35], 0, v[176:177]
	v_lshl_add_u64 v[38:39], v[34:35], 0, s[22:23]
	v_add_co_u32_e32 v34, vcc, s69, v34
	v_add_u32_e32 v48, s4, v42
	s_nop 0
	v_addc_co_u32_e32 v35, vcc, 0, v35, vcc
	global_load_dwordx4 v[44:47], v[34:35], off
	global_load_dwordx4 v[40:43], v[38:39], off offset:128
	v_lshl_add_u32 v34, v48, 6, v199
	v_ashrrev_i32_e32 v35, 31, v34
	v_lshlrev_b64 v[38:39], 2, v[34:35]
	v_lshl_add_u64 v[48:49], v[32:33], 0, v[38:39]
	global_load_dwordx4 v[32:35], v[48:49], off offset:16
	global_load_dwordx4 v[64:67], v[48:49], off
	v_lshl_add_u64 v[48:49], v[36:37], 0, v[38:39]
	global_load_dwordx4 v[36:39], v[48:49], off offset:16
	global_load_dwordx4 v[68:71], v[48:49], off
	v_add_u32_e32 v48, s9, v97
	v_mad_i64_i32 v[48:49], s[38:39], v48, s67, v[56:57]
	v_lshl_add_u64 v[48:49], v[48:49], 0, v[180:181]
	v_mov_b32_e32 v97, v177
	v_add_u32_e32 v52, s9, v99
	v_lshl_add_u64 v[48:49], v[48:49], 0, v[96:97]
	v_mad_i64_i32 v[52:53], s[38:39], v52, s67, v[56:57]
	v_add_co_u32_e32 v48, vcc, s69, v48
	v_lshl_add_u64 v[52:53], v[52:53], 0, v[180:181]
	v_add_u32_e32 v58, s9, v100
	v_addc_co_u32_e32 v49, vcc, 0, v49, vcc
	v_lshl_add_u64 v[52:53], v[52:53], 0, v[96:97]
	v_mad_i64_i32 v[58:59], s[38:39], v58, s67, v[56:57]
	v_add_co_u32_e32 v52, vcc, s69, v52
	v_lshl_add_u64 v[58:59], v[58:59], 0, v[180:181]
	s_nop 0
	v_addc_co_u32_e32 v53, vcc, 0, v53, vcc
	v_lshl_add_u64 v[58:59], v[58:59], 0, v[96:97]
	v_add_co_u32_e32 v58, vcc, s69, v58
	v_and_b32_e32 v118, 16, v102
	s_nop 0
	v_addc_co_u32_e32 v59, vcc, 0, v59, vcc
	global_load_dwordx4 v[60:63], v[58:59], off offset:1024
	v_add_u32_e32 v58, s9, v101
	v_mad_i64_i32 v[56:57], s[38:39], v58, s67, v[56:57]
	v_lshl_add_u64 v[56:57], v[56:57], 0, v[180:181]
	v_lshl_add_u64 v[56:57], v[56:57], 0, v[96:97]
	v_bfe_u32 v97, v98, 2, 4
	v_add_co_u32_e32 v56, vcc, s69, v56
	v_and_b32_e32 v116, 8, v102
	v_add_u32_e32 v96, s77, v118
	v_mul_u32_u24_e32 v117, 0x120, v97
	v_lshrrev_b32_e32 v114, 2, v98
	v_addc_co_u32_e32 v57, vcc, 0, v57, vcc
	v_add3_u32 v120, v96, v116, v117
	s_movk_i32 s9, 0x7e
	global_load_dwordx4 v[48:51], v[48:49], off offset:1024
	v_bitop3_b32 v100, v114, s66, 12 bitop3:0x6c
	global_load_dwordx4 v[52:55], v[52:53], off offset:1024
	v_bitop3_b32 v101, v114, s9, 12 bitop3:0x6c
	global_load_dwordx4 v[56:59], v[56:57], off offset:1024
	ds_read_b64_tr_b16 v[98:99], v120 offset:36864
	ds_read_b64_tr_b16 v[96:97], v120 offset:41472
	v_cvt_f32_ubyte0_e32 v100, v100
	v_cvt_f32_ubyte0_e32 v101, v101
	v_mul_f32_e32 v100, v115, v100
	v_mul_f32_e32 v101, v115, v101
	v_exp_f32_e32 v100, v100
	v_exp_f32_e32 v101, v101
	s_movk_i32 s9, 0x7d
	s_waitcnt lgkmcnt(1)
	v_lshlrev_b32_e32 v102, 16, v98
	v_and_b32_e32 v103, 0xffff0000, v98
	v_bitop3_b32 v98, v114, s9, 12 bitop3:0x6c
	v_cvt_f32_ubyte0_e32 v98, v98
	v_mul_f32_e32 v98, v115, v98
	s_movk_i32 s9, 0x7c
	v_pk_mul_f32 v[100:101], v[100:101], v[102:103]
	v_exp_f32_e32 v102, v98
	v_bitop3_b32 v98, v114, s9, 12 bitop3:0x6c
	v_cvt_f32_ubyte0_e32 v98, v98
	v_mul_f32_e32 v98, v115, v98
	v_exp_f32_e32 v103, v98
	v_lshlrev_b32_e32 v98, 16, v99
	v_and_b32_e32 v99, 0xffff0000, v99
	s_movk_i32 s9, 0x6f
	v_pk_mul_f32 v[98:99], v[102:103], v[98:99]
	v_bitop3_b32 v102, v114, s9, 12 bitop3:0x6c
	s_movk_i32 s9, 0x6e
	v_bitop3_b32 v103, v114, s9, 12 bitop3:0x6c
	v_cvt_f32_ubyte0_e32 v102, v102
	v_cvt_f32_ubyte0_e32 v103, v103
	v_mul_f32_e32 v102, v115, v102
	v_mul_f32_e32 v103, v115, v103
	v_exp_f32_e32 v102, v102
	v_exp_f32_e32 v103, v103
	s_movk_i32 s9, 0x6d
	s_waitcnt lgkmcnt(0)
	v_lshlrev_b32_e32 v104, 16, v96
	v_and_b32_e32 v105, 0xffff0000, v96
	v_bitop3_b32 v96, v114, s9, 12 bitop3:0x6c
	v_cvt_f32_ubyte0_e32 v96, v96
	v_mul_f32_e32 v96, v115, v96
	s_movk_i32 s9, 0x6c
	v_pk_mul_f32 v[102:103], v[102:103], v[104:105]
	v_exp_f32_e32 v104, v96
	v_bitop3_b32 v96, v114, s9, 12 bitop3:0x6c
	v_cvt_f32_ubyte0_e32 v96, v96
	v_mul_f32_e32 v96, v115, v96
	v_exp_f32_e32 v105, v96
	v_lshlrev_b32_e32 v96, 16, v97
	v_and_b32_e32 v97, 0xffff0000, v97
	s_movk_i32 s9, 0x5f
	v_pk_mul_f32 v[104:105], v[104:105], v[96:97]
	v_cvt_pk_bf16_f32 v97, v98, v99
	v_cvt_pk_bf16_f32 v98, v102, v103
	v_bitop3_b32 v102, v114, s9, 12 bitop3:0x6c
	s_movk_i32 s9, 0x5e
	v_cvt_pk_bf16_f32 v96, v100, v101
	v_cvt_pk_bf16_f32 v99, v104, v105
	ds_read_b64_tr_b16 v[104:105], v120 offset:46080
	ds_read_b64_tr_b16 v[100:101], v120 offset:50688
	v_bitop3_b32 v103, v114, s9, 12 bitop3:0x6c
	v_cvt_f32_ubyte0_e32 v102, v102
	v_cvt_f32_ubyte0_e32 v103, v103
	v_mul_f32_e32 v102, v115, v102
	v_mul_f32_e32 v103, v115, v103
	v_exp_f32_e32 v102, v102
	v_exp_f32_e32 v103, v103
	s_movk_i32 s9, 0x5d
	s_waitcnt lgkmcnt(1)
; __device__ __forceinline__ bf16x8 pack8(const float (&f)[8]) { u32x4 u; u.x = cvtpk(f[0], f[1]); u.y = cvtpk(f[2], f[3]); u.z = cvtpk(f[4], f[5]); u.w = cvtpk(f[6], f[7]); return __builtin_bit_cast(bf16x8, u); }
; template <bool FWD> __device__ __forceinline__ void state_update_1(LAS unsigned char* lds, f32x4 (&racc)[8], float l2, int w, int g, unsigned qp, unsigned p) {
;     const float dec = __builtin_amdgcn_exp2f(128.f * l2);
;     bf16x8 vs[4];
; #pragma unroll
;     for (int ks = 0; ks < 4; ++ks) {
;         float f[8]; unpack8(trfrag(lds + LV, 32 * ks + 4 * g, 32 * ks + 16 + 4 * g, w, qp, p), f);
; #pragma unroll
;         for (int e = 0; e < 8; ++e) { const int key = 32 * ks + 16 * (e >> 2) + 4 * g + (e & 3); f[e] *= __builtin_amdgcn_exp2f((FWD ? (float)(127 - key) : (float)key) * l2); }
;         vs[ks] = pack8(f);
;     }
; #pragma unroll
;     for (int nb = 0; nb < 8; ++nb) {
;         racc[nb] = racc[nb] * dec;
; #pragma unroll
;         for (int ks = 0; ks < 4; ++ks) racc[nb] = __builtin_amdgcn_mfma_f32_16x16x32_bf16(vs[ks], trfrag(lds + LK, 32 * ks + 4 * g, 32 * ks + 16 + 4 * g, nb, qp, p), racc[nb], 0, 0, 0);
;     }
	v_lshlrev_b32_e32 v106, 16, v104
	v_and_b32_e32 v107, 0xffff0000, v104
	v_bitop3_b32 v104, v114, s9, 12 bitop3:0x6c
	v_cvt_f32_ubyte0_e32 v104, v104
	v_mul_f32_e32 v104, v115, v104
	s_movk_i32 s9, 0x5c
	v_pk_mul_f32 v[102:103], v[102:103], v[106:107]
	v_exp_f32_e32 v106, v104
	v_bitop3_b32 v104, v114, s9, 12 bitop3:0x6c
	v_cvt_f32_ubyte0_e32 v104, v104
	v_mul_f32_e32 v104, v115, v104
	v_exp_f32_e32 v107, v104
	v_lshlrev_b32_e32 v104, 16, v105
	v_and_b32_e32 v105, 0xffff0000, v105
	s_movk_i32 s9, 0x4f
	v_pk_mul_f32 v[106:107], v[106:107], v[104:105]
	v_bitop3_b32 v104, v114, s9, 12 bitop3:0x6c
	s_movk_i32 s9, 0x4e
	v_bitop3_b32 v105, v114, s9, 12 bitop3:0x6c
	v_cvt_f32_ubyte0_e32 v104, v104
	v_cvt_f32_ubyte0_e32 v105, v105
	v_mul_f32_e32 v104, v115, v104
	v_mul_f32_e32 v105, v115, v105
	v_exp_f32_e32 v104, v104
	v_exp_f32_e32 v105, v105
	s_movk_i32 s9, 0x4d
	s_waitcnt lgkmcnt(0)
	v_lshlrev_b32_e32 v108, 16, v100
	v_and_b32_e32 v109, 0xffff0000, v100
	v_bitop3_b32 v100, v114, s9, 12 bitop3:0x6c
	v_cvt_f32_ubyte0_e32 v100, v100
	v_mul_f32_e32 v100, v115, v100
	s_movk_i32 s9, 0x4c
	v_pk_mul_f32 v[108:109], v[104:105], v[108:109]
	v_exp_f32_e32 v104, v100
	v_bitop3_b32 v100, v114, s9, 12 bitop3:0x6c
	v_cvt_f32_ubyte0_e32 v100, v100
	v_mul_f32_e32 v100, v115, v100
	v_exp_f32_e32 v105, v100
	v_lshlrev_b32_e32 v100, 16, v101
	v_and_b32_e32 v101, 0xffff0000, v101
	v_bitop3_b32 v121, v114, 30, 12 bitop3:0x6c
	v_pk_mul_f32 v[100:101], v[104:105], v[100:101]
	v_cvt_pk_bf16_f32 v104, v102, v103
	v_cvt_pk_bf16_f32 v105, v106, v107
	v_cvt_pk_bf16_f32 v106, v108, v109
	v_cvt_pk_bf16_f32 v107, v100, v101
	ds_read_b64_tr_b16 v[100:101], v120 offset:55296
	ds_read_b64_tr_b16 v[102:103], v120 offset:59904
	v_bitop3_b32 v108, v114, 63, 12 bitop3:0x6c
	v_bitop3_b32 v109, v114, 62, 12 bitop3:0x6c
	v_cvt_f32_ubyte0_e32 v108, v108
	v_cvt_f32_ubyte0_e32 v109, v109
	v_mul_f32_e32 v108, v115, v108
	v_mul_f32_e32 v109, v115, v109
	v_exp_f32_e32 v108, v108
	v_exp_f32_e32 v109, v109
	s_waitcnt lgkmcnt(1)
	v_lshlrev_b32_e32 v110, 16, v100
	v_and_b32_e32 v111, 0xffff0000, v100
	v_bitop3_b32 v100, v114, 61, 12 bitop3:0x6c
	v_cvt_f32_ubyte0_e32 v100, v100
	v_mul_f32_e32 v100, v115, v100
	v_pk_mul_f32 v[108:109], v[108:109], v[110:111]
	v_exp_f32_e32 v110, v100
	v_bitop3_b32 v100, v114, 60, 12 bitop3:0x6c
	v_cvt_f32_ubyte0_e32 v100, v100
	v_mul_f32_e32 v100, v115, v100
	v_exp_f32_e32 v111, v100
	v_lshlrev_b32_e32 v100, 16, v101
	v_and_b32_e32 v101, 0xffff0000, v101
	s_waitcnt lgkmcnt(0)
	v_lshlrev_b32_e32 v122, 16, v102
	v_pk_mul_f32 v[100:101], v[110:111], v[100:101]
	v_bitop3_b32 v110, v114, 47, 12 bitop3:0x6c
	v_bitop3_b32 v111, v114, 46, 12 bitop3:0x6c
	v_cvt_f32_ubyte0_e32 v110, v110
	v_cvt_f32_ubyte0_e32 v111, v111
	v_mul_f32_e32 v110, v115, v110
	v_mul_f32_e32 v111, v115, v111
	v_exp_f32_e32 v110, v110
	v_exp_f32_e32 v111, v111
	v_and_b32_e32 v123, 0xffff0000, v102
	v_bitop3_b32 v102, v114, 45, 12 bitop3:0x6c
	v_cvt_f32_ubyte0_e32 v102, v102
	v_mul_f32_e32 v102, v115, v102
	v_pk_mul_f32 v[110:111], v[110:111], v[122:123]
	v_exp_f32_e32 v122, v102
	v_bitop3_b32 v102, v114, 44, 12 bitop3:0x6c
	v_cvt_f32_ubyte0_e32 v102, v102
	v_mul_f32_e32 v102, v115, v102
	v_exp_f32_e32 v123, v102
	v_lshlrev_b32_e32 v102, 16, v103
	v_and_b32_e32 v103, 0xffff0000, v103
	v_cvt_pk_bf16_f32 v110, v110, v111
	v_pk_mul_f32 v[102:103], v[122:123], v[102:103]
	v_cvt_pk_bf16_f32 v108, v108, v109
	v_cvt_pk_bf16_f32 v111, v102, v103
	v_add_u32_e32 v102, 0xfc00, v120
	v_cvt_pk_bf16_f32 v109, v100, v101
	ds_read_b64_tr_b16 v[100:101], v120 offset:64512
	ds_read_b64_tr_b16 v[102:103], v102 offset:4608
	v_bitop3_b32 v120, v114, 31, 12 bitop3:0x6c
	v_cvt_f32_ubyte0_e32 v120, v120
	v_cvt_f32_ubyte0_e32 v121, v121
	v_mul_f32_e32 v120, v115, v120
	v_mul_f32_e32 v121, v115, v121
	v_exp_f32_e32 v120, v120
	v_exp_f32_e32 v121, v121
	s_waitcnt lgkmcnt(1)
	v_lshlrev_b32_e32 v122, 16, v100
	v_and_b32_e32 v123, 0xffff0000, v100
	v_bitop3_b32 v100, v114, 29, 12 bitop3:0x6c
	v_cvt_f32_ubyte0_e32 v100, v100
	v_mul_f32_e32 v100, v115, v100
	v_pk_mul_f32 v[120:121], v[120:121], v[122:123]
	v_exp_f32_e32 v122, v100
	v_bitop3_b32 v100, v114, 28, 12 bitop3:0x6c
	v_cvt_f32_ubyte0_e32 v100, v100
	v_mul_f32_e32 v100, v115, v100
	v_exp_f32_e32 v123, v100
	v_lshlrev_b32_e32 v100, 16, v101
	v_and_b32_e32 v101, 0xffff0000, v101
	s_waitcnt lgkmcnt(0)
	v_lshlrev_b32_e32 v124, 16, v102
	v_pk_mul_f32 v[122:123], v[122:123], v[100:101]
	v_bitop3_b32 v100, v114, 15, 12 bitop3:0x6c
	v_bitop3_b32 v101, v114, 14, 12 bitop3:0x6c
	v_cvt_f32_ubyte0_e32 v100, v100
	v_cvt_f32_ubyte0_e32 v101, v101
	v_mul_f32_e32 v100, v115, v100
	v_mul_f32_e32 v101, v115, v101
	v_exp_f32_e32 v100, v100
	v_exp_f32_e32 v101, v101
	v_and_b32_e32 v125, 0xffff0000, v102
	v_lshlrev_b32_e32 v102, 16, v103
	v_and_b32_e32 v103, 0xffff0000, v103
	v_pk_mul_f32 v[124:125], v[100:101], v[124:125]
	v_bitop3_b32 v100, v114, 13, 12 bitop3:0x6c
	v_bitop3_b32 v101, v114, 12, v114 bitop3:0xc
	v_cvt_f32_ubyte0_e32 v100, v100
	v_cvt_f32_ubyte0_e32 v101, v101
	v_mul_f32_e32 v100, v115, v100
	v_mul_f32_e32 v101, v115, v101
	v_exp_f32_e32 v100, v100
	v_exp_f32_e32 v101, v101
	v_mul_f32_e32 v119, 0x43000000, v115
	s_addk_i32 s4, 0x80
	s_cmp_eq_u32 s8, s4
	v_pk_mul_f32 v[114:115], v[100:101], v[102:103]
	v_cvt_pk_bf16_f32 v100, v120, v121
	v_cvt_pk_bf16_f32 v103, v114, v115
	v_exp_f32_e32 v114, v119
	v_add_u32_e32 v115, 0, v118
	v_cvt_pk_bf16_f32 v101, v122, v123
	v_cvt_pk_bf16_f32 v102, v124, v125
	v_pk_mul_f32 v[22:23], v[22:23], v[114:115] op_sel_hi:[1,0]
	v_pk_mul_f32 v[20:21], v[20:21], v[114:115] op_sel_hi:[1,0]
	v_add3_u32 v115, v115, v116, v117
	ds_read_b64_tr_b16 v[222:223], v115
	ds_read_b64_tr_b16 v[224:225], v115 offset:4608
	ds_read_b64_tr_b16 v[226:227], v115 offset:9216
	ds_read_b64_tr_b16 v[228:229], v115 offset:13824
	ds_read_b64_tr_b16 v[236:237], v115 offset:18432
	ds_read_b64_tr_b16 v[238:239], v115 offset:23040
	ds_read_b64_tr_b16 v[240:241], v115 offset:27648
	ds_read_b64_tr_b16 v[242:243], v115 offset:32256
	s_waitcnt lgkmcnt(6)
; template <bool FWD> __device__ __forceinline__ void state_update_1(LAS unsigned char* lds, f32x4 (&racc)[8], float l2, int w, int g, unsigned qp, unsigned p) {
;     ...
; #pragma unroll
;     for (int nb = 0; nb < 8; ++nb) {
;         racc[nb] = racc[nb] * dec;
; #pragma unroll
;         for (int ks = 0; ks < 4; ++ks) racc[nb] = __builtin_amdgcn_mfma_f32_16x16x32_bf16(vs[ks], trfrag(lds + LK, 32 * ks + 4 * g, 32 * ks + 16 + 4 * g, nb, qp, p), racc[nb], 0, 0, 0);
;     }
	v_mfma_f32_16x16x32_bf16 v[20:23], v[96:99], v[222:225], v[20:23]
	v_pk_mul_f32 v[2:3], v[2:3], v[114:115] op_sel_hi:[1,0]
	v_pk_mul_f32 v[0:1], v[0:1], v[114:115] op_sel_hi:[1,0]
	ds_read_b64_tr_b16 v[222:223], v115 offset:32
	ds_read_b64_tr_b16 v[224:225], v115 offset:4640
	s_waitcnt lgkmcnt(6)
	v_mfma_f32_16x16x32_bf16 v[20:23], v[104:107], v[226:229], v[20:23]
	v_pk_mul_f32 v[18:19], v[18:19], v[114:115] op_sel_hi:[1,0]
	v_pk_mul_f32 v[16:17], v[16:17], v[114:115] op_sel_hi:[1,0]
	ds_read_b64_tr_b16 v[226:227], v115 offset:9248
	ds_read_b64_tr_b16 v[228:229], v115 offset:13856
	s_waitcnt lgkmcnt(6)
	v_mfma_f32_16x16x32_bf16 v[20:23], v[108:111], v[236:239], v[20:23]
	v_pk_mul_f32 v[26:27], v[26:27], v[114:115] op_sel_hi:[1,0]
	ds_read_b64_tr_b16 v[236:237], v115 offset:18464
	ds_read_b64_tr_b16 v[238:239], v115 offset:23072
	s_waitcnt lgkmcnt(6)
	v_mfma_f32_16x16x32_bf16 v[20:23], v[100:103], v[240:243], v[20:23]
	v_pk_mul_f32 v[24:25], v[24:25], v[114:115] op_sel_hi:[1,0]
	v_pk_mul_f32 v[6:7], v[6:7], v[114:115] op_sel_hi:[1,0]
	ds_read_b64_tr_b16 v[240:241], v115 offset:27680
	ds_read_b64_tr_b16 v[242:243], v115 offset:32288
	s_waitcnt lgkmcnt(6)
	v_mfma_f32_16x16x32_bf16 v[0:3], v[96:99], v[222:225], v[0:3]
	v_mul_f32_e64 v4, v4, v114
	v_mul_f32_e64 v5, v5, v114
	v_pk_mul_f32 v[10:11], v[10:11], v[114:115] op_sel_hi:[1,0]
	v_pk_mul_f32 v[8:9], v[8:9], v[114:115] op_sel_hi:[1,0]
	ds_read_b64_tr_b16 v[222:223], v115 offset:64
	ds_read_b64_tr_b16 v[224:225], v115 offset:4672
	s_waitcnt lgkmcnt(6)
	v_mfma_f32_16x16x32_bf16 v[0:3], v[104:107], v[226:229], v[0:3]
	v_pk_mul_f32 v[14:15], v[14:15], v[114:115] op_sel_hi:[1,0]
	v_pk_mul_f32 v[12:13], v[12:13], v[114:115] op_sel_hi:[1,0]
	ds_read_b64_tr_b16 v[226:227], v115 offset:9280
	ds_read_b64_tr_b16 v[228:229], v115 offset:13888
	s_waitcnt lgkmcnt(6)
	v_mfma_f32_16x16x32_bf16 v[0:3], v[108:111], v[236:239], v[0:3]
	v_pk_mul_f32 v[30:31], v[30:31], v[114:115] op_sel_hi:[1,0]
	v_pk_mul_f32 v[28:29], v[28:29], v[114:115] op_sel_hi:[1,0]
	ds_read_b64_tr_b16 v[236:237], v115 offset:18496
	ds_read_b64_tr_b16 v[238:239], v115 offset:23104
	s_waitcnt lgkmcnt(6)
	v_mfma_f32_16x16x32_bf16 v[0:3], v[100:103], v[240:243], v[0:3]
	ds_read_b64_tr_b16 v[240:241], v115 offset:27712
	ds_read_b64_tr_b16 v[242:243], v115 offset:32320
	s_waitcnt lgkmcnt(6)
	v_mfma_f32_16x16x32_bf16 v[16:19], v[96:99], v[222:225], v[16:19]
	ds_read_b64_tr_b16 v[222:223], v115 offset:96
	ds_read_b64_tr_b16 v[224:225], v115 offset:4704
	s_waitcnt lgkmcnt(6)
	v_mfma_f32_16x16x32_bf16 v[16:19], v[104:107], v[226:229], v[16:19]
	ds_read_b64_tr_b16 v[226:227], v115 offset:9312
	ds_read_b64_tr_b16 v[228:229], v115 offset:13920
	s_waitcnt lgkmcnt(6)
	v_mfma_f32_16x16x32_bf16 v[16:19], v[108:111], v[236:239], v[16:19]
	ds_read_b64_tr_b16 v[236:237], v115 offset:18528
	ds_read_b64_tr_b16 v[238:239], v115 offset:23136
	s_waitcnt lgkmcnt(6)
	v_mfma_f32_16x16x32_bf16 v[16:19], v[100:103], v[240:243], v[16:19]
	ds_read_b64_tr_b16 v[240:241], v115 offset:27744
	ds_read_b64_tr_b16 v[242:243], v115 offset:32352
	s_waitcnt lgkmcnt(6)
	v_mfma_f32_16x16x32_bf16 v[24:27], v[96:99], v[222:225], v[24:27]
	ds_read_b64_tr_b16 v[222:223], v115 offset:128
	ds_read_b64_tr_b16 v[224:225], v115 offset:4736
	s_waitcnt lgkmcnt(6)
	v_mfma_f32_16x16x32_bf16 v[24:27], v[104:107], v[226:229], v[24:27]
	ds_read_b64_tr_b16 v[226:227], v115 offset:9344
	ds_read_b64_tr_b16 v[228:229], v115 offset:13952
	s_waitcnt lgkmcnt(6)
	v_mfma_f32_16x16x32_bf16 v[24:27], v[108:111], v[236:239], v[24:27]
	ds_read_b64_tr_b16 v[236:237], v115 offset:18560
	ds_read_b64_tr_b16 v[238:239], v115 offset:23168
	s_waitcnt lgkmcnt(6)
	v_mfma_f32_16x16x32_bf16 v[24:27], v[100:103], v[240:243], v[24:27]
	ds_read_b64_tr_b16 v[240:241], v115 offset:27776
	ds_read_b64_tr_b16 v[242:243], v115 offset:32384
	s_waitcnt lgkmcnt(6)
	v_mfma_f32_16x16x32_bf16 v[4:7], v[96:99], v[222:225], v[4:7]
	ds_read_b64_tr_b16 v[222:223], v115 offset:160
	ds_read_b64_tr_b16 v[224:225], v115 offset:4768
	s_waitcnt lgkmcnt(6)
	v_mfma_f32_16x16x32_bf16 v[4:7], v[104:107], v[226:229], v[4:7]
	ds_read_b64_tr_b16 v[226:227], v115 offset:9376
	ds_read_b64_tr_b16 v[228:229], v115 offset:13984
	s_waitcnt lgkmcnt(6)
	v_mfma_f32_16x16x32_bf16 v[4:7], v[108:111], v[236:239], v[4:7]
	ds_read_b64_tr_b16 v[236:237], v115 offset:18592
	ds_read_b64_tr_b16 v[238:239], v115 offset:23200
	s_waitcnt lgkmcnt(6)
	v_mfma_f32_16x16x32_bf16 v[4:7], v[100:103], v[240:243], v[4:7]
	ds_read_b64_tr_b16 v[240:241], v115 offset:27808
	ds_read_b64_tr_b16 v[242:243], v115 offset:32416
	s_waitcnt lgkmcnt(6)
	v_mfma_f32_16x16x32_bf16 v[8:11], v[96:99], v[222:225], v[8:11]
	ds_read_b64_tr_b16 v[222:223], v115 offset:192
	ds_read_b64_tr_b16 v[224:225], v115 offset:4800
	s_waitcnt lgkmcnt(6)
	v_mfma_f32_16x16x32_bf16 v[8:11], v[104:107], v[226:229], v[8:11]
	ds_read_b64_tr_b16 v[226:227], v115 offset:9408
	ds_read_b64_tr_b16 v[228:229], v115 offset:14016
	s_waitcnt lgkmcnt(6)
	v_mfma_f32_16x16x32_bf16 v[8:11], v[108:111], v[236:239], v[8:11]
	ds_read_b64_tr_b16 v[236:237], v115 offset:18624
	ds_read_b64_tr_b16 v[238:239], v115 offset:23232
	s_waitcnt lgkmcnt(6)
	v_mfma_f32_16x16x32_bf16 v[8:11], v[100:103], v[240:243], v[8:11]
	ds_read_b64_tr_b16 v[240:241], v115 offset:27840
	ds_read_b64_tr_b16 v[242:243], v115 offset:32448
	s_waitcnt lgkmcnt(6)
	v_mfma_f32_16x16x32_bf16 v[12:15], v[96:99], v[222:225], v[12:15]
	ds_read_b64_tr_b16 v[222:223], v115 offset:224
	ds_read_b64_tr_b16 v[224:225], v115 offset:4832
	s_waitcnt lgkmcnt(6)
	v_mfma_f32_16x16x32_bf16 v[12:15], v[104:107], v[226:229], v[12:15]
	ds_read_b64_tr_b16 v[226:227], v115 offset:9440
	ds_read_b64_tr_b16 v[228:229], v115 offset:14048
	s_waitcnt lgkmcnt(6)
	v_mfma_f32_16x16x32_bf16 v[12:15], v[108:111], v[236:239], v[12:15]
	ds_read_b64_tr_b16 v[236:237], v115 offset:18656
	ds_read_b64_tr_b16 v[238:239], v115 offset:23264
	s_waitcnt lgkmcnt(6)
	v_mfma_f32_16x16x32_bf16 v[12:15], v[100:103], v[240:243], v[12:15]
	ds_read_b64_tr_b16 v[240:241], v115 offset:27872
	ds_read_b64_tr_b16 v[242:243], v115 offset:32480
	s_waitcnt lgkmcnt(6)
	v_mfma_f32_16x16x32_bf16 v[28:31], v[96:99], v[222:225], v[28:31]
	s_waitcnt lgkmcnt(4)
	v_mfma_f32_16x16x32_bf16 v[28:31], v[104:107], v[226:229], v[28:31]
	s_waitcnt lgkmcnt(2)
	v_mfma_f32_16x16x32_bf16 v[28:31], v[108:111], v[236:239], v[28:31]
	s_waitcnt lgkmcnt(0)
	v_mfma_f32_16x16x32_bf16 v[28:31], v[100:103], v[240:243], v[28:31]
	s_cbranch_scc0 .LBB0_287
	s_branch .LBB0_289

; __device__ __forceinline__ void unit(const bf16_t* __restrict__ proj, const float* __restrict__ rope, const float* __restrict__ log_decay, const float* __restrict__ gn_g, bf16_t* __restrict__ ymix, ...
;     ...
;         { float s = 0.f;
; #pragma unroll
;           for (int mbv = 0; mbv < 8; ++mbv) s += (yacc[mbv][0] + yacc[mbv][1]) + (yacc[mbv][2] + yacc[mbv][3]);
;           s += __shfl_xor(s, 16); s += __shfl_xor(s, 32);
;           const float mu = s * (1.f / 128.f); float s2 = 0.f;
; #pragma unroll
;           for (int mbv = 0; mbv < 8; ++mbv) { yacc[mbv] = yacc[mbv] - mu; s2 += (yacc[mbv][0] * yacc[mbv][0] + yacc[mbv][1] * yacc[mbv][1]) + (yacc[mbv][2] * yacc[mbv][2] + yacc[mbv][3] * yacc[mbv][3]); }
;           s2 += __shfl_xor(s2, 16); s2 += __shfl_xor(s2, 32);
.LBB0_300:
	v_mov_b32_e32 v116, v144
	v_mov_b32_e32 v117, v112
	v_mov_b32_e32 v118, v145
	v_mov_b32_e32 v119, v113
	v_pk_add_f32 v[116:117], v[116:117], v[118:119]
	v_mov_b32_e32 v118, v146
	v_mov_b32_e32 v119, v114
	v_mov_b32_e32 v120, v147
	v_mov_b32_e32 v121, v115
	v_pk_add_f32 v[118:119], v[118:119], v[120:121]
	v_mov_b32_e32 v120, v140
	v_pk_add_f32 v[116:117], v[116:117], v[118:119]
	v_mov_b32_e32 v118, v141
	v_mov_b32_e32 v119, v142
	v_mov_b32_e32 v121, v143
	v_pk_add_f32 v[118:119], v[118:119], v[120:121]
	v_add_f32_e32 v116, 0, v116
	v_pk_add_f32 v[118:119], v[118:119], v[118:119] op_sel:[0,1] op_sel_hi:[1,0]
	v_add_f32_e32 v116, v116, v117
	v_add_f32_e32 v120, v132, v133
	v_add_f32_e32 v122, v134, v135
	v_mov_b32_e32 v117, v104
	v_mov_b32_e32 v119, v105
	v_mov_b32_e32 v121, v106
	v_mov_b32_e32 v123, v107
	v_pk_add_f32 v[116:117], v[116:117], v[118:119]
	v_pk_add_f32 v[118:119], v[120:121], v[122:123]
	v_mov_b32_e32 v120, v100
	v_pk_add_f32 v[116:117], v[116:117], v[118:119]
	v_mov_b32_e32 v118, v101
	v_mov_b32_e32 v119, v102
	v_mov_b32_e32 v121, v103
	v_pk_add_f32 v[118:119], v[118:119], v[120:121]
	v_pk_add_f32 v[116:117], v[116:117], v[116:117] op_sel:[0,1] op_sel_hi:[1,0]
	v_pk_add_f32 v[118:119], v[118:119], v[118:119] op_sel:[0,1] op_sel_hi:[1,0]
	v_add_f32_e32 v120, v96, v97
	v_add_f32_e32 v122, v98, v99
	v_mov_b32_e32 v117, v108
	v_mov_b32_e32 v119, v109
	v_mov_b32_e32 v121, v110
	v_mov_b32_e32 v123, v111
	v_pk_add_f32 v[116:117], v[116:117], v[118:119]
	v_pk_add_f32 v[118:119], v[120:121], v[122:123]
	v_ashrrev_i32_e32 v187, 31, v186
	v_pk_add_f32 v[116:117], v[116:117], v[118:119]
	v_mov_b32_e32 v185, v177
	v_add_f32_e32 v116, v116, v117
	ds_bpermute_b32 v117, v195, v116
	s_add_i32 s5, s5, 1
	s_add_u32 s60, s60, 0x9000
	s_addc_u32 s61, s61, 0
	s_addk_i32 s84, 0x80
	s_waitcnt lgkmcnt(0)
	v_add_f32_e32 v116, v116, v117
	ds_bpermute_b32 v117, v196, v116
	s_cmp_lg_u32 s60, 0x48000
	s_waitcnt lgkmcnt(0)
	v_add_f32_e32 v116, v116, v117
	v_fmamk_f32 v138, v116, 0xbc000000, v147
	v_fmac_f32_e32 v145, 0xbc000000, v116
	v_fmamk_f32 v131, v116, 0xbc000000, v115
	v_fmac_f32_e32 v113, 0xbc000000, v116
	v_fmamk_f32 v137, v116, 0xbc000000, v146
	v_fmamk_f32 v139, v116, 0xbc000000, v144
	v_mul_f32_e32 v117, v145, v145
	v_mul_f32_e32 v118, v138, v138
	v_fmamk_f32 v136, v116, 0xbc000000, v114
	v_fmamk_f32 v144, v116, 0xbc000000, v112
	v_mul_f32_e32 v112, v113, v113
	v_mul_f32_e32 v114, v131, v131
	v_fmac_f32_e32 v117, v139, v139
	v_fmac_f32_e32 v118, v137, v137
	v_fmac_f32_e32 v112, v144, v144
	v_fmac_f32_e32 v114, v136, v136
	v_add_f32_e32 v117, v117, v118
	v_add_f32_e32 v112, v112, v114
	v_add_f32_e32 v114, v117, v112
	v_fmamk_f32 v112, v116, 0xbc000000, v143
	v_fmac_f32_e32 v141, 0xbc000000, v116
	v_fmamk_f32 v129, v116, 0xbc000000, v142
	v_fmamk_f32 v130, v116, 0xbc000000, v140
	v_mul_f32_e32 v115, v141, v141
	v_mul_f32_e32 v117, v112, v112
	v_fmac_f32_e32 v115, v130, v130
	v_fmac_f32_e32 v117, v129, v129
	v_add_f32_e32 v115, v115, v117
	v_fmamk_f32 v126, v116, 0xbc000000, v135
	v_fmac_f32_e32 v133, 0xbc000000, v116
	v_add_f32_e32 v114, v115, v114
	v_fmamk_f32 v127, v116, 0xbc000000, v134
	v_fmamk_f32 v128, v116, 0xbc000000, v132
	v_mul_f32_e32 v115, v133, v133
	v_mul_f32_e32 v117, v126, v126
	v_fmamk_f32 v124, v116, 0xbc000000, v107
	v_fmac_f32_e32 v105, 0xbc000000, v116
	v_fmac_f32_e32 v115, v128, v128
	v_fmac_f32_e32 v117, v127, v127
	v_fmamk_f32 v125, v116, 0xbc000000, v106
	v_fmamk_f32 v104, v116, 0xbc000000, v104
	v_mul_f32_e32 v106, v105, v105
	v_mul_f32_e32 v107, v124, v124
	v_fmamk_f32 v121, v116, 0xbc000000, v103
	v_fmac_f32_e32 v101, 0xbc000000, v116
	v_add_f32_e32 v115, v115, v117
	v_fmac_f32_e32 v106, v104, v104
	v_fmac_f32_e32 v107, v125, v125
	v_fmamk_f32 v122, v116, 0xbc000000, v102
	v_fmamk_f32 v123, v116, 0xbc000000, v100
	v_mul_f32_e32 v100, v101, v101
	v_mul_f32_e32 v102, v121, v121
	v_fmamk_f32 v118, v116, 0xbc000000, v99
	v_fmac_f32_e32 v97, 0xbc000000, v116
	v_add_f32_e32 v114, v115, v114
	v_add_f32_e32 v106, v106, v107
	v_fmac_f32_e32 v100, v123, v123
	v_fmac_f32_e32 v102, v122, v122
	v_fmamk_f32 v119, v116, 0xbc000000, v98
	v_fmamk_f32 v120, v116, 0xbc000000, v96
	v_mul_f32_e32 v96, v97, v97
	v_mul_f32_e32 v98, v118, v118
	v_add_f32_e32 v106, v106, v114
	v_add_f32_e32 v100, v100, v102
	v_fmac_f32_e32 v96, v120, v120
	v_fmac_f32_e32 v98, v119, v119
	v_add_f32_e32 v100, v100, v106
	v_add_f32_e32 v96, v96, v98
	v_add_f32_e32 v98, v96, v100
	v_fmamk_f32 v96, v116, 0xbc000000, v111
	v_fmac_f32_e32 v109, 0xbc000000, v116
	v_fmamk_f32 v100, v116, 0xbc000000, v110
	v_fmamk_f32 v106, v116, 0xbc000000, v108
	v_mul_f32_e32 v99, v109, v109
	v_mul_f32_e32 v102, v96, v96
	v_fmac_f32_e32 v99, v106, v106
	v_fmac_f32_e32 v102, v100, v100
	v_add_f32_e32 v99, v99, v102
	v_add_f32_e32 v98, v99, v98
	ds_bpermute_b32 v99, v195, v98
	s_waitcnt vmcnt(0)
	v_lshlrev_b32_e32 v110, 16, v191
	v_and_b32_e32 v111, 0xffff0000, v191
	s_waitcnt lgkmcnt(0)
	v_add_f32_e32 v98, v98, v99
	ds_bpermute_b32 v99, v196, v98
	s_waitcnt lgkmcnt(0)
; #define LAS __attribute__((address_space(3)))
; __device__ __forceinline__ float silu_f(float v) { return v * __builtin_amdgcn_rcpf(1.f + __expf(-v)); }
; __device__ __forceinline__ float clamp8(float v) { return __builtin_amdgcn_fmed3f(v, -440.f, 440.f); }
; __device__ __forceinline__ void unit(const bf16_t* __restrict__ proj, const float* __restrict__ rope, const float* __restrict__ log_decay, const float* __restrict__ gn_g, bf16_t* __restrict__ ymix, ...
;     ...
;           const float rstd = 1.f / sqrtf(s2 * (1.f / 128.f) + GN_EPS);
;           unsigned char* op = (unsigned char*)ymix + (size_t)(b * SEQ + tq) * D + 512 + h * 128 + 4 * g;
; #pragma unroll
;           for (int rep4 = 0; rep4 < (RET_PROBE == 4 ? 2 : 1); ++rep4) {
;           if (RET_PROBE == 4) { asm volatile("" : "+v"(op)); asm volatile("" : "+v"(gv[0]), "+v"(gv[1]), "+v"(gv[2]), "+v"(gv[3]), "+v"(gv[4]), "+v"(gv[5]), "+v"(gv[6]), "+v"(gv[7])); }
; #pragma unroll
;           for (int mbv = 0; mbv < 8; ++mbv) {
;               const f32x4 gn = *(const LAS f32x4*)(gnp + 16 * mbv + 4 * g);
;               const float g0 = __uint_as_float(gv[mbv].x << 16), g1 = __uint_as_float(gv[mbv].x & 0xffff0000u), g2 = __uint_as_float(gv[mbv].y << 16), g3 = __uint_as_float(gv[mbv].y & 0xffff0000u);
;               int o = __builtin_amdgcn_cvt_pk_fp8_f32(clamp8(S_H8 * silu_f(g0) * (yacc[mbv][0] * rstd * gn.x)), clamp8(S_H8 * silu_f(g1) * (yacc[mbv][1] * rstd * gn.y)), 0, false);
;               o = __builtin_amdgcn_cvt_pk_fp8_f32(clamp8(S_H8 * silu_f(g2) * (yacc[mbv][2] * rstd * gn.z)), clamp8(S_H8 * silu_f(g3) * (yacc[mbv][3] * rstd * gn.w)), o, true);
;               *(unsigned*)(op + 16 * mbv) = (unsigned)o;
	v_add_f32_e32 v98, v98, v99
	v_fmamk_f32 v98, v98, 0x3c000000, v197
	v_cmp_gt_f32_e32 vcc, s71, v98
	v_mul_f32_e32 v99, 0x4f800000, v98
	s_nop 0
	v_cndmask_b32_e32 v98, v98, v99, vcc
	v_sqrt_f32_e32 v99, v98
	s_nop 0
	v_add_u32_e32 v102, -1, v99
	v_fma_f32 v103, -v102, v99, v98
	v_cmp_ge_f32_e64 s[8:9], 0, v103
	v_add_u32_e32 v103, 1, v99
	s_nop 0
	v_cndmask_b32_e64 v102, v99, v102, s[8:9]
	v_fma_f32 v99, -v103, v99, v98
	v_cmp_lt_f32_e64 s[8:9], 0, v99
	s_nop 1
	v_cndmask_b32_e64 v99, v102, v103, s[8:9]
	v_mul_f32_e32 v102, 0x37800000, v99
	v_cndmask_b32_e32 v99, v99, v102, vcc
	v_cmp_class_f32_e32 vcc, v98, v198
	s_nop 1
	v_cndmask_b32_e32 v98, v99, v98, vcc
	v_div_scale_f32 v99, s[8:9], v98, v98, 1.0
	v_rcp_f32_e32 v102, v99
	s_nop 0
	v_fma_f32 v103, -v99, v102, 1.0
	v_fmac_f32_e32 v102, v103, v102
	v_div_scale_f32 v103, vcc, 1.0, v98, 1.0
	v_mul_f32_e32 v107, v103, v102
	v_fma_f32 v108, -v99, v107, v103
	v_fmac_f32_e32 v107, v108, v102
	v_fma_f32 v99, -v99, v107, v103
	v_div_fmas_f32 v99, v99, v102, v107
	v_lshlrev_b32_e32 v102, 16, v190
	v_mul_f32_e32 v132, 0xbfb8aa3b, v102
	v_exp_f32_e32 v132, v132
	v_lshl_add_u32 v108, v184, 2, v206
	ds_read_b128 v[114:117], v108
	v_div_fixup_f32 v107, v99, v98, 1.0
	v_add_f32_e32 v132, 1.0, v132
	v_rcp_f32_e32 v132, v132
	v_and_b32_e32 v103, 0xffff0000, v190
	v_lshlrev_b64 v[98:99], 10, v[186:187]
	v_lshl_add_u64 v[98:99], v[182:183], 0, v[98:99]
	v_mul_f32_e32 v102, v132, v102
	v_mul_f32_e32 v132, v139, v107
	v_mul_f32_e32 v102, 0x41800000, v102
	s_waitcnt lgkmcnt(0)
	v_mul_f32_e32 v114, v114, v132
	v_mul_f32_e32 v102, v102, v114
	v_mul_f32_e32 v114, 0xbfb8aa3b, v103
	v_exp_f32_e32 v114, v114
	v_med3_f32 v102, v102, s72, v200
	v_lshl_add_u64 v[98:99], v[98:99], 0, v[184:185]
	v_mul_f32_e32 v113, v113, v107
	v_add_f32_e32 v114, 1.0, v114
	v_rcp_f32_e32 v114, v114
	v_mul_f32_e32 v104, v104, v107
	v_mul_f32_e32 v101, v101, v107
	v_mul_f32_e32 v97, v97, v107
	v_mul_f32_e32 v103, v114, v103
	v_mul_f32_e32 v114, v145, v107
	v_mul_f32_e32 v103, 0x41800000, v103
	v_mul_f32_e32 v114, v115, v114
	v_mul_f32_e32 v103, v103, v114
	v_med3_f32 v103, v103, s72, v200
	v_mov_b32_e32 v114, v177
	v_cvt_pk_fp8_f32 v114, v102, v103
	v_mul_f32_e32 v102, 0xbfb8aa3b, v110
	v_exp_f32_e32 v102, v102
	v_mul_f32_e32 v103, v137, v107
	v_mul_f32_e32 v103, v116, v103
	v_mul_f32_e32 v106, v106, v107
	v_add_f32_e32 v102, 1.0, v102
	v_rcp_f32_e32 v102, v102
	v_mul_f32_e32 v100, v100, v107
	v_mul_f32_e32 v96, v96, v107
	v_mul_f32_e32 v102, v102, v110
	v_mul_f32_e32 v102, 0x41800000, v102
	v_mul_f32_e32 v102, v102, v103
	v_mul_f32_e32 v103, 0xbfb8aa3b, v111
	v_exp_f32_e32 v103, v103
	v_mul_f32_e32 v110, v138, v107
	v_mul_f32_e32 v110, v117, v110
	v_med3_f32 v102, v102, s72, v200
	v_add_f32_e32 v103, 1.0, v103
	v_rcp_f32_e32 v103, v103
	s_nop 0
	v_mul_f32_e32 v103, v103, v111
	v_mul_f32_e32 v103, 0x41800000, v103
	v_mul_f32_e32 v103, v103, v110
	v_med3_f32 v103, v103, s72, v200
	v_cvt_pk_fp8_f32 v114, v102, v103 op_sel:[0,0,1]
	v_lshlrev_b32_e32 v102, 16, v188
	v_mul_f32_e32 v132, 0xbfb8aa3b, v102
	v_exp_f32_e32 v132, v132
	global_store_dword v[98:99], v114, off offset:512
	ds_read_b128 v[114:117], v108 offset:64
	v_and_b32_e32 v103, 0xffff0000, v188
	v_add_f32_e32 v132, 1.0, v132
	v_rcp_f32_e32 v132, v132
	v_lshlrev_b32_e32 v110, 16, v189
	s_waitcnt lgkmcnt(0)
	v_mul_f32_e32 v113, v115, v113
	v_and_b32_e32 v111, 0xffff0000, v189
	v_mul_f32_e32 v102, v132, v102
	v_mul_f32_e32 v132, v144, v107
	v_mul_f32_e32 v102, 0x41800000, v102
	v_mul_f32_e32 v114, v114, v132
	v_mul_f32_e32 v102, v102, v114
	v_mul_f32_e32 v114, 0xbfb8aa3b, v103
	v_exp_f32_e32 v114, v114
	v_med3_f32 v102, v102, s72, v200
	v_add_f32_e32 v114, 1.0, v114
	v_rcp_f32_e32 v114, v114
	s_nop 0
	v_mul_f32_e32 v103, v114, v103
	v_mul_f32_e32 v103, 0x41800000, v103
	v_mul_f32_e32 v103, v103, v113
	v_med3_f32 v103, v103, s72, v200
	v_mov_b32_e32 v113, v177
	v_cvt_pk_fp8_f32 v113, v102, v103
	v_mul_f32_e32 v102, 0xbfb8aa3b, v110
	v_exp_f32_e32 v102, v102
	v_mul_f32_e32 v103, v136, v107
	v_mul_f32_e32 v103, v116, v103
	v_add_f32_e32 v102, 1.0, v102
	v_rcp_f32_e32 v102, v102
	s_nop 0
	v_mul_f32_e32 v102, v102, v110
	v_mul_f32_e32 v102, 0x41800000, v102
	v_mul_f32_e32 v102, v102, v103
	v_mul_f32_e32 v103, 0xbfb8aa3b, v111
	v_exp_f32_e32 v103, v103
	v_mul_f32_e32 v110, v131, v107
	v_mul_f32_e32 v110, v117, v110
	v_med3_f32 v102, v102, s72, v200
	v_add_f32_e32 v103, 1.0, v103
	v_rcp_f32_e32 v103, v103
	ds_read_b128 v[114:117], v108 offset:128
	v_mul_f32_e32 v103, v103, v111
	v_mul_f32_e32 v103, 0x41800000, v103
	v_mul_f32_e32 v103, v103, v110
	v_med3_f32 v103, v103, s72, v200
	v_cvt_pk_fp8_f32 v113, v102, v103 op_sel:[0,0,1]
	v_lshlrev_b32_e32 v102, 16, v172
	v_and_b32_e32 v103, 0xffff0000, v172
	v_lshlrev_b32_e32 v110, 16, v173
	global_store_dword v[98:99], v113, off offset:528
	v_mul_f32_e32 v113, 0xbfb8aa3b, v102
	v_exp_f32_e32 v113, v113
	v_and_b32_e32 v111, 0xffff0000, v173
	v_add_f32_e32 v113, 1.0, v113
	v_rcp_f32_e32 v113, v113
	s_nop 0
	v_mul_f32_e32 v102, v113, v102
	v_mul_f32_e32 v113, v130, v107
	v_mul_f32_e32 v102, 0x41800000, v102
	s_waitcnt lgkmcnt(0)
; #define LAS __attribute__((address_space(3)))
; __device__ __forceinline__ float silu_f(float v) { return v * __builtin_amdgcn_rcpf(1.f + __expf(-v)); }
; __device__ __forceinline__ float clamp8(float v) { return __builtin_amdgcn_fmed3f(v, -440.f, 440.f); }
; __device__ __forceinline__ void unit(const bf16_t* __restrict__ proj, const float* __restrict__ rope, const float* __restrict__ log_decay, const float* __restrict__ gn_g, bf16_t* __restrict__ ymix, ...
;     ...
; #pragma unroll
;           for (int mbv = 0; mbv < 8; ++mbv) {
;               const f32x4 gn = *(const LAS f32x4*)(gnp + 16 * mbv + 4 * g);
;               const float g0 = __uint_as_float(gv[mbv].x << 16), g1 = __uint_as_float(gv[mbv].x & 0xffff0000u), g2 = __uint_as_float(gv[mbv].y << 16), g3 = __uint_as_float(gv[mbv].y & 0xffff0000u);
;               int o = __builtin_amdgcn_cvt_pk_fp8_f32(clamp8(S_H8 * silu_f(g0) * (yacc[mbv][0] * rstd * gn.x)), clamp8(S_H8 * silu_f(g1) * (yacc[mbv][1] * rstd * gn.y)), 0, false);
;               o = __builtin_amdgcn_cvt_pk_fp8_f32(clamp8(S_H8 * silu_f(g2) * (yacc[mbv][2] * rstd * gn.z)), clamp8(S_H8 * silu_f(g3) * (yacc[mbv][3] * rstd * gn.w)), o, true);
;               *(unsigned*)(op + 16 * mbv) = (unsigned)o;
;           } } }
	v_mul_f32_e32 v113, v114, v113
	v_mul_f32_e32 v102, v102, v113
	v_mul_f32_e32 v113, 0xbfb8aa3b, v103
	v_exp_f32_e32 v113, v113
	v_med3_f32 v102, v102, s72, v200
	v_lshlrev_b32_e32 v114, 16, v171
	v_add_f32_e32 v113, 1.0, v113
	v_rcp_f32_e32 v113, v113
	s_nop 0
	v_mul_f32_e32 v103, v113, v103
	v_mul_f32_e32 v113, v141, v107
	v_mul_f32_e32 v103, 0x41800000, v103
	v_mul_f32_e32 v113, v115, v113
	v_mul_f32_e32 v103, v103, v113
	v_med3_f32 v103, v103, s72, v200
	v_mov_b32_e32 v113, v177
	v_cvt_pk_fp8_f32 v113, v102, v103
	v_mul_f32_e32 v102, 0xbfb8aa3b, v110
	v_exp_f32_e32 v102, v102
	v_mul_f32_e32 v103, v129, v107
	v_mul_f32_e32 v103, v116, v103
	v_and_b32_e32 v115, 0xffff0000, v171
	v_add_f32_e32 v102, 1.0, v102
	v_rcp_f32_e32 v102, v102
	s_nop 0
	v_mul_f32_e32 v102, v102, v110
	v_mul_f32_e32 v102, 0x41800000, v102
	v_mul_f32_e32 v102, v102, v103
	v_mul_f32_e32 v103, 0xbfb8aa3b, v111
	v_exp_f32_e32 v103, v103
	v_mul_f32_e32 v110, v112, v107
	v_mul_f32_e32 v110, v117, v110
	v_med3_f32 v102, v102, s72, v200
	v_add_f32_e32 v103, 1.0, v103
	v_rcp_f32_e32 v103, v103
	s_nop 0
	v_mul_f32_e32 v103, v103, v111
	v_mul_f32_e32 v103, 0x41800000, v103
	v_mul_f32_e32 v103, v103, v110
	v_med3_f32 v103, v103, s72, v200
	v_cvt_pk_fp8_f32 v113, v102, v103 op_sel:[0,0,1]
	v_lshlrev_b32_e32 v102, 16, v170
	v_mul_f32_e32 v116, 0xbfb8aa3b, v102
	v_exp_f32_e32 v116, v116
	global_store_dword v[98:99], v113, off offset:544
	ds_read_b128 v[110:113], v108 offset:192
	v_and_b32_e32 v103, 0xffff0000, v170
	v_add_f32_e32 v116, 1.0, v116
	v_rcp_f32_e32 v116, v116
	s_nop 0
	v_mul_f32_e32 v102, v116, v102
	v_mul_f32_e32 v116, v128, v107
	v_mul_f32_e32 v102, 0x41800000, v102
	s_waitcnt lgkmcnt(0)
	v_mul_f32_e32 v110, v110, v116
	v_mul_f32_e32 v102, v102, v110
	v_mul_f32_e32 v110, 0xbfb8aa3b, v103
	v_exp_f32_e32 v110, v110
	v_med3_f32 v102, v102, s72, v200
	v_add_f32_e32 v110, 1.0, v110
	v_rcp_f32_e32 v110, v110
	s_nop 0
	v_mul_f32_e32 v103, v110, v103
	v_mul_f32_e32 v110, v133, v107
	v_mul_f32_e32 v103, 0x41800000, v103
	v_mul_f32_e32 v110, v111, v110
	v_mul_f32_e32 v103, v103, v110
	v_med3_f32 v103, v103, s72, v200
	v_mov_b32_e32 v110, v177
	v_cvt_pk_fp8_f32 v110, v102, v103
	v_mul_f32_e32 v102, 0xbfb8aa3b, v114
	v_exp_f32_e32 v102, v102
	v_mul_f32_e32 v103, v127, v107
	v_mul_f32_e32 v103, v112, v103
	v_mul_f32_e32 v111, v126, v107
	v_add_f32_e32 v102, 1.0, v102
	v_rcp_f32_e32 v102, v102
	v_mul_f32_e32 v111, v113, v111
	v_mul_f32_e32 v102, v102, v114
	v_mul_f32_e32 v102, 0x41800000, v102
	v_mul_f32_e32 v102, v102, v103
	v_mul_f32_e32 v103, 0xbfb8aa3b, v115
	v_exp_f32_e32 v103, v103
	v_med3_f32 v102, v102, s72, v200
	v_lshlrev_b32_e32 v114, 16, v169
	v_add_f32_e32 v103, 1.0, v103
	v_rcp_f32_e32 v103, v103
	s_nop 0
	v_mul_f32_e32 v103, v103, v115
	v_mul_f32_e32 v103, 0x41800000, v103
	v_mul_f32_e32 v103, v103, v111
	v_med3_f32 v103, v103, s72, v200
	v_cvt_pk_fp8_f32 v110, v102, v103 op_sel:[0,0,1]
	v_lshlrev_b32_e32 v102, 16, v168
	v_mul_f32_e32 v116, 0xbfb8aa3b, v102
	v_exp_f32_e32 v116, v116
	global_store_dword v[98:99], v110, off offset:560
	ds_read_b128 v[110:113], v108 offset:256
	v_and_b32_e32 v103, 0xffff0000, v168
	v_add_f32_e32 v116, 1.0, v116
	v_rcp_f32_e32 v116, v116
	v_and_b32_e32 v115, 0xffff0000, v169
	s_waitcnt lgkmcnt(0)
	v_mul_f32_e32 v104, v110, v104
	v_lshlrev_b32_e32 v110, 16, v156
	v_mul_f32_e32 v102, v116, v102
	v_mul_f32_e32 v102, 0x41800000, v102
	v_mul_f32_e32 v102, v102, v104
	v_mul_f32_e32 v104, 0xbfb8aa3b, v103
	v_exp_f32_e32 v104, v104
	v_med3_f32 v102, v102, s72, v200
	v_add_f32_e32 v104, 1.0, v104
	v_rcp_f32_e32 v104, v104
	s_nop 0
	v_mul_f32_e32 v103, v104, v103
	v_mul_f32_e32 v104, v105, v107
	v_mul_f32_e32 v103, 0x41800000, v103
	v_mul_f32_e32 v104, v111, v104
	v_mul_f32_e32 v103, v103, v104
	v_med3_f32 v103, v103, s72, v200
	v_mov_b32_e32 v104, v177
	v_cvt_pk_fp8_f32 v104, v102, v103
	v_mul_f32_e32 v102, 0xbfb8aa3b, v114
	v_exp_f32_e32 v102, v102
	v_mul_f32_e32 v103, v125, v107
	v_mul_f32_e32 v103, v112, v103
	v_mul_f32_e32 v105, v124, v107
	v_add_f32_e32 v102, 1.0, v102
	v_rcp_f32_e32 v102, v102
	v_mul_f32_e32 v105, v113, v105
	v_and_b32_e32 v111, 0xffff0000, v156
	v_lshlrev_b32_e32 v112, 16, v157
	v_mul_f32_e32 v102, v102, v114
	v_mul_f32_e32 v102, 0x41800000, v102
	v_mul_f32_e32 v102, v102, v103
	v_mul_f32_e32 v103, 0xbfb8aa3b, v115
	v_exp_f32_e32 v103, v103
	v_mul_f32_e32 v114, 0xbfb8aa3b, v110
	v_med3_f32 v102, v102, s72, v200
	v_exp_f32_e32 v114, v114
	v_add_f32_e32 v103, 1.0, v103
	v_rcp_f32_e32 v103, v103
	v_and_b32_e32 v113, 0xffff0000, v157
	v_add_f32_e32 v114, 1.0, v114
	v_rcp_f32_e32 v114, v114
	v_mul_f32_e32 v103, v103, v115
	v_mul_f32_e32 v103, 0x41800000, v103
	v_mul_f32_e32 v103, v103, v105
	v_med3_f32 v103, v103, s72, v200
	v_cvt_pk_fp8_f32 v104, v102, v103 op_sel:[0,0,1]
	v_mul_f32_e32 v110, v114, v110
	v_mul_f32_e32 v114, v123, v107
	v_mul_f32_e32 v110, 0x41800000, v110
	global_store_dword v[98:99], v104, off offset:576
	ds_read_b128 v[102:105], v108 offset:320
	s_waitcnt lgkmcnt(0)
; #define LAS __attribute__((address_space(3)))
; __device__ __forceinline__ float silu_f(float v) { return v * __builtin_amdgcn_rcpf(1.f + __expf(-v)); }
; __device__ __forceinline__ float clamp8(float v) { return __builtin_amdgcn_fmed3f(v, -440.f, 440.f); }
; __device__ __forceinline__ bf16x8 pack8(const float (&f)[8]) { u32x4 u; u.x = cvtpk(f[0], f[1]); u.y = cvtpk(f[2], f[3]); u.z = cvtpk(f[4], f[5]); u.w = cvtpk(f[6], f[7]); return __builtin_bit_cast(bf16x8, u); }
; template <bool FWD> __device__ __forceinline__ void state_update_1(LAS unsigned char* lds, f32x4 (&racc)[8], float l2, int w, int g, unsigned qp, unsigned p) {
;     const float dec = __builtin_amdgcn_exp2f(128.f * l2);
;     bf16x8 vs[4];
; #pragma unroll
;     for (int ks = 0; ks < 4; ++ks) {
;         float f[8]; unpack8(trfrag(lds + LV, 32 * ks + 4 * g, 32 * ks + 16 + 4 * g, w, qp, p), f);
; #pragma unroll
;         for (int e = 0; e < 8; ++e) { const int key = 32 * ks + 16 * (e >> 2) + 4 * g + (e & 3); f[e] *= __builtin_amdgcn_exp2f((FWD ? (float)(127 - key) : (float)key) * l2); }
;         vs[ks] = pack8(f);
;     }
; __device__ __forceinline__ void unit(const bf16_t* __restrict__ proj, const float* __restrict__ rope, const float* __restrict__ log_decay, const float* __restrict__ gn_g, bf16_t* __restrict__ ymix, ...
;     ...
; #pragma unroll
;           for (int mbv = 0; mbv < 8; ++mbv) {
;               const f32x4 gn = *(const LAS f32x4*)(gnp + 16 * mbv + 4 * g);
;               const float g0 = __uint_as_float(gv[mbv].x << 16), g1 = __uint_as_float(gv[mbv].x & 0xffff0000u), g2 = __uint_as_float(gv[mbv].y << 16), g3 = __uint_as_float(gv[mbv].y & 0xffff0000u);
;               int o = __builtin_amdgcn_cvt_pk_fp8_f32(clamp8(S_H8 * silu_f(g0) * (yacc[mbv][0] * rstd * gn.x)), clamp8(S_H8 * silu_f(g1) * (yacc[mbv][1] * rstd * gn.y)), 0, false);
;               o = __builtin_amdgcn_cvt_pk_fp8_f32(clamp8(S_H8 * silu_f(g2) * (yacc[mbv][2] * rstd * gn.z)), clamp8(S_H8 * silu_f(g3) * (yacc[mbv][3] * rstd * gn.w)), o, true);
;               *(unsigned*)(op + 16 * mbv) = (unsigned)o;
;           } } }
	v_mul_f32_e32 v102, v102, v114
	v_mul_f32_e32 v102, v110, v102
	v_mul_f32_e32 v110, 0xbfb8aa3b, v111
	v_exp_f32_e32 v110, v110
	v_mul_f32_e32 v101, v103, v101
	v_med3_f32 v102, v102, s72, v200
	v_mov_b32_e32 v103, v177
	v_add_f32_e32 v110, 1.0, v110
	v_rcp_f32_e32 v110, v110
	s_nop 0
	v_mul_f32_e32 v110, v110, v111
	v_mul_f32_e32 v110, 0x41800000, v110
	v_mul_f32_e32 v101, v110, v101
	v_med3_f32 v101, v101, s72, v200
	v_cvt_pk_fp8_f32 v103, v102, v101
	v_mul_f32_e32 v101, 0xbfb8aa3b, v112
	v_exp_f32_e32 v101, v101
	v_mul_f32_e32 v102, v122, v107
	v_mul_f32_e32 v102, v104, v102
	v_mul_f32_e32 v104, v121, v107
	v_add_f32_e32 v101, 1.0, v101
	v_rcp_f32_e32 v101, v101
	v_mul_f32_e32 v104, v105, v104
	v_and_b32_e32 v110, 0xffff0000, v154
	v_lshlrev_b32_e32 v111, 16, v155
	v_mul_f32_e32 v101, v101, v112
	v_mul_f32_e32 v101, 0x41800000, v101
	v_mul_f32_e32 v101, v101, v102
	v_mul_f32_e32 v102, 0xbfb8aa3b, v113
	v_exp_f32_e32 v102, v102
	v_med3_f32 v101, v101, s72, v200
	v_and_b32_e32 v112, 0xffff0000, v155
	v_add_f32_e32 v102, 1.0, v102
	v_rcp_f32_e32 v102, v102
	s_nop 0
	v_mul_f32_e32 v102, v102, v113
	v_mul_f32_e32 v102, 0x41800000, v102
	v_mul_f32_e32 v102, v102, v104
	v_med3_f32 v102, v102, s72, v200
	v_cvt_pk_fp8_f32 v103, v101, v102 op_sel:[0,0,1]
	v_lshlrev_b32_e32 v101, 16, v154
	v_mul_f32_e32 v113, 0xbfb8aa3b, v101
	v_exp_f32_e32 v113, v113
	global_store_dword v[98:99], v103, off offset:592
	ds_read_b128 v[102:105], v108 offset:384
	v_add_f32_e32 v113, 1.0, v113
	v_rcp_f32_e32 v113, v113
	s_waitcnt lgkmcnt(0)
	v_mul_f32_e32 v97, v97, v103
	v_mul_f32_e32 v103, v118, v107
	v_mul_f32_e32 v101, v113, v101
	v_mul_f32_e32 v113, v120, v107
	v_mul_f32_e32 v101, 0x41800000, v101
	v_mul_f32_e32 v102, v113, v102
	v_mul_f32_e32 v101, v101, v102
	v_mul_f32_e32 v102, 0xbfb8aa3b, v110
	v_exp_f32_e32 v102, v102
	v_med3_f32 v101, v101, s72, v200
	v_mul_f32_e32 v103, v103, v105
	v_xor_b32_e32 v113, 31, v184
	v_add_f32_e32 v102, 1.0, v102
	v_rcp_f32_e32 v102, v102
	v_cvt_f32_ubyte0_e32 v113, v113
	v_mul_f32_e32 v113, v204, v113
	v_mul_f32_e32 v102, v102, v110
	v_mul_f32_e32 v102, 0x41800000, v102
	v_mul_f32_e32 v97, v102, v97
	v_med3_f32 v97, v97, s72, v200
	v_mov_b32_e32 v102, v177
	v_cvt_pk_fp8_f32 v102, v101, v97
	v_mul_f32_e32 v97, 0xbfb8aa3b, v111
	v_exp_f32_e32 v97, v97
	v_mul_f32_e32 v101, v119, v107
	v_mul_f32_e32 v101, v101, v104
	v_and_b32_e32 v110, 0xffff0000, v153
	v_add_f32_e32 v97, 1.0, v97
	v_rcp_f32_e32 v97, v97
	s_nop 0
	v_mul_f32_e32 v97, v97, v111
	v_mul_f32_e32 v97, 0x41800000, v97
	v_mul_f32_e32 v97, v97, v101
	v_mul_f32_e32 v101, 0xbfb8aa3b, v112
	v_exp_f32_e32 v101, v101
	v_med3_f32 v97, v97, s72, v200
	v_add_f32_e32 v101, 1.0, v101
	v_rcp_f32_e32 v101, v101
	s_nop 0
	v_mul_f32_e32 v101, v101, v112
	v_mul_f32_e32 v101, 0x41800000, v101
	v_mul_f32_e32 v101, v101, v103
	v_med3_f32 v101, v101, s72, v200
	v_cvt_pk_fp8_f32 v102, v97, v101 op_sel:[0,0,1]
	v_lshlrev_b32_e32 v97, 16, v152
	v_mul_f32_e32 v111, 0xbfb8aa3b, v97
	v_exp_f32_e32 v111, v111
	global_store_dword v[98:99], v102, off offset:608
	ds_read_b128 v[102:105], v108 offset:448
	v_and_b32_e32 v101, 0xffff0000, v152
	v_add_f32_e32 v111, 1.0, v111
	v_rcp_f32_e32 v111, v111
	v_lshlrev_b32_e32 v108, 16, v153
	s_waitcnt lgkmcnt(0)
	v_mul_f32_e32 v102, v106, v102
	v_mul_f32_e32 v100, v100, v104
	v_mul_f32_e32 v97, v111, v97
	v_mul_f32_e32 v97, 0x41800000, v97
	v_mul_f32_e32 v97, v97, v102
	v_mul_f32_e32 v102, 0xbfb8aa3b, v101
	v_exp_f32_e32 v102, v102
	v_med3_f32 v97, v97, s72, v200
	v_mul_f32_e32 v96, v96, v105
	v_mul_f32_e32 v112, 0x43000000, v204
	v_add_f32_e32 v102, 1.0, v102
	v_rcp_f32_e32 v102, v102
	v_exp_f32_e32 v112, v112
	v_mul_f32_e32 v101, v102, v101
	v_mul_f32_e32 v102, v109, v107
	v_mul_f32_e32 v101, 0x41800000, v101
	v_mul_f32_e32 v102, v102, v103
	v_mul_f32_e32 v101, v101, v102
	v_med3_f32 v101, v101, s72, v200
	v_mov_b32_e32 v102, v177
	v_cvt_pk_fp8_f32 v102, v97, v101
	v_mul_f32_e32 v97, 0xbfb8aa3b, v108
	v_exp_f32_e32 v97, v97
	v_sub_u32_e32 v101, 0x7e, v184
	v_cvt_f32_ubyte0_e32 v101, v101
	v_mul_f32_e32 v101, v204, v101
	v_add_f32_e32 v97, 1.0, v97
	v_rcp_f32_e32 v97, v97
	v_exp_f32_e32 v101, v101
	v_xor_b32_e32 v109, 63, v184
	v_cvt_f32_ubyte0_e32 v109, v109
	v_mul_f32_e32 v97, v97, v108
	v_mul_f32_e32 v97, 0x41800000, v97
	v_mul_f32_e32 v97, v97, v100
	v_mul_f32_e32 v100, 0xbfb8aa3b, v110
	v_exp_f32_e32 v100, v100
	v_med3_f32 v97, v97, s72, v200
	v_mul_f32_e32 v109, v204, v109
	v_add_f32_e32 v100, 1.0, v100
	v_rcp_f32_e32 v100, v100
	s_nop 0
	v_mul_f32_e32 v100, v100, v110
	v_mul_f32_e32 v100, 0x41800000, v100
	v_mul_f32_e32 v96, v100, v96
	v_med3_f32 v96, v96, s72, v200
	v_cvt_pk_fp8_f32 v102, v97, v96 op_sel:[0,0,1]
	v_add_u32_e32 v96, s77, v208
	v_add3_u32 v108, v96, v207, v209
	v_xor_b32_e32 v100, 0x7f, v184
	global_store_dword v[98:99], v102, off offset:624
	ds_read_b64_tr_b16 v[96:97], v108 offset:36864
	ds_read_b64_tr_b16 v[98:99], v108 offset:41472
	v_cvt_f32_ubyte0_e32 v100, v100
	v_mul_f32_e32 v100, v204, v100
	v_exp_f32_e32 v100, v100
	s_waitcnt lgkmcnt(1)
	v_lshlrev_b32_e32 v102, 16, v96
	v_and_b32_e32 v103, 0xffff0000, v96
	v_sub_u32_e32 v96, 0x7d, v184
	v_cvt_f32_ubyte0_e32 v96, v96
	v_mul_f32_e32 v96, v204, v96
	v_pk_mul_f32 v[100:101], v[100:101], v[102:103]
	v_exp_f32_e32 v102, v96
	v_sub_u32_e32 v96, 0x7c, v184
	v_cvt_f32_ubyte0_e32 v96, v96
	v_mul_f32_e32 v96, v204, v96
	v_exp_f32_e32 v103, v96
	v_lshlrev_b32_e32 v96, 16, v97
	v_and_b32_e32 v97, 0xffff0000, v97
	s_waitcnt lgkmcnt(0)
; __device__ __forceinline__ bf16x8 pack8(const float (&f)[8]) { u32x4 u; u.x = cvtpk(f[0], f[1]); u.y = cvtpk(f[2], f[3]); u.z = cvtpk(f[4], f[5]); u.w = cvtpk(f[6], f[7]); return __builtin_bit_cast(bf16x8, u); }
; template <bool FWD> __device__ __forceinline__ void state_update_1(LAS unsigned char* lds, f32x4 (&racc)[8], float l2, int w, int g, unsigned qp, unsigned p) {
;     const float dec = __builtin_amdgcn_exp2f(128.f * l2);
;     bf16x8 vs[4];
; #pragma unroll
;     for (int ks = 0; ks < 4; ++ks) {
;         float f[8]; unpack8(trfrag(lds + LV, 32 * ks + 4 * g, 32 * ks + 16 + 4 * g, w, qp, p), f);
; #pragma unroll
;         for (int e = 0; e < 8; ++e) { const int key = 32 * ks + 16 * (e >> 2) + 4 * g + (e & 3); f[e] *= __builtin_amdgcn_exp2f((FWD ? (float)(127 - key) : (float)key) * l2); }
;         vs[ks] = pack8(f);
;     }
	v_lshlrev_b32_e32 v104, 16, v98
	v_pk_mul_f32 v[102:103], v[102:103], v[96:97]
	v_xor_b32_e32 v96, 0x6f, v184
	v_sub_u32_e32 v97, 0x6e, v184
	v_cvt_f32_ubyte0_e32 v96, v96
	v_cvt_f32_ubyte0_e32 v97, v97
	v_mul_f32_e32 v96, v204, v96
	v_mul_f32_e32 v97, v204, v97
	v_exp_f32_e32 v96, v96
	v_exp_f32_e32 v97, v97
	v_and_b32_e32 v105, 0xffff0000, v98
	v_lshlrev_b32_e32 v98, 16, v99
	v_and_b32_e32 v99, 0xffff0000, v99
	v_pk_mul_f32 v[104:105], v[96:97], v[104:105]
	v_sub_u32_e32 v96, 0x6d, v184
	v_sub_u32_e32 v97, 0x6c, v184
	v_cvt_f32_ubyte0_e32 v96, v96
	v_cvt_f32_ubyte0_e32 v97, v97
	v_mul_f32_e32 v96, v204, v96
	v_mul_f32_e32 v97, v204, v97
	v_exp_f32_e32 v96, v96
	v_exp_f32_e32 v97, v97
	s_nop 0
	v_pk_mul_f32 v[106:107], v[96:97], v[98:99]
	v_cvt_pk_bf16_f32 v96, v100, v101
	v_cvt_pk_bf16_f32 v97, v102, v103
	v_cvt_pk_bf16_f32 v98, v104, v105
	ds_read_b64_tr_b16 v[100:101], v108 offset:46080
	ds_read_b64_tr_b16 v[102:103], v108 offset:50688
	v_xor_b32_e32 v104, 0x5f, v184
	v_sub_u32_e32 v105, 0x5e, v184
	v_cvt_f32_ubyte0_e32 v104, v104
	v_cvt_f32_ubyte0_e32 v105, v105
	v_mul_f32_e32 v104, v204, v104
	v_mul_f32_e32 v105, v204, v105
	v_exp_f32_e32 v104, v104
	v_exp_f32_e32 v105, v105
	v_cvt_pk_bf16_f32 v99, v106, v107
	s_waitcnt lgkmcnt(1)
	v_lshlrev_b32_e32 v106, 16, v100
	v_and_b32_e32 v107, 0xffff0000, v100
	v_sub_u32_e32 v100, 0x5d, v184
	v_cvt_f32_ubyte0_e32 v100, v100
	v_mul_f32_e32 v100, v204, v100
	v_pk_mul_f32 v[104:105], v[104:105], v[106:107]
	v_exp_f32_e32 v106, v100
	v_sub_u32_e32 v100, 0x5c, v184
	v_cvt_f32_ubyte0_e32 v100, v100
	v_mul_f32_e32 v100, v204, v100
	v_exp_f32_e32 v107, v100
	v_lshlrev_b32_e32 v100, 16, v101
	v_and_b32_e32 v101, 0xffff0000, v101
	s_waitcnt lgkmcnt(0)
	v_lshlrev_b32_e32 v110, 16, v102
	v_pk_mul_f32 v[106:107], v[106:107], v[100:101]
	v_xor_b32_e32 v100, 0x4f, v184
	v_sub_u32_e32 v101, 0x4e, v184
	v_cvt_f32_ubyte0_e32 v100, v100
	v_cvt_f32_ubyte0_e32 v101, v101
	v_mul_f32_e32 v100, v204, v100
	v_mul_f32_e32 v101, v204, v101
	v_exp_f32_e32 v100, v100
	v_exp_f32_e32 v101, v101
	v_and_b32_e32 v111, 0xffff0000, v102
	v_lshlrev_b32_e32 v102, 16, v103
	v_and_b32_e32 v103, 0xffff0000, v103
	v_pk_mul_f32 v[110:111], v[100:101], v[110:111]
	v_sub_u32_e32 v100, 0x4d, v184
	v_sub_u32_e32 v101, 0x4c, v184
	v_cvt_f32_ubyte0_e32 v100, v100
	v_cvt_f32_ubyte0_e32 v101, v101
	v_mul_f32_e32 v100, v204, v100
	v_mul_f32_e32 v101, v204, v101
	v_exp_f32_e32 v100, v100
	v_exp_f32_e32 v101, v101
	s_nop 0
	v_pk_mul_f32 v[114:115], v[100:101], v[102:103]
	v_cvt_pk_bf16_f32 v100, v104, v105
	v_cvt_pk_bf16_f32 v101, v106, v107
	v_cvt_pk_bf16_f32 v102, v110, v111
	ds_read_b64_tr_b16 v[104:105], v108 offset:55296
	ds_read_b64_tr_b16 v[106:107], v108 offset:59904
	v_exp_f32_e32 v110, v109
	v_sub_u32_e32 v109, 62, v184
	v_cvt_f32_ubyte0_e32 v109, v109
	v_mul_f32_e32 v109, v204, v109
	v_exp_f32_e32 v111, v109
	v_cvt_pk_bf16_f32 v103, v114, v115
	s_waitcnt lgkmcnt(1)
	v_lshlrev_b32_e32 v114, 16, v104
	v_and_b32_e32 v115, 0xffff0000, v104
	v_sub_u32_e32 v104, 61, v184
	v_cvt_f32_ubyte0_e32 v104, v104
	v_mul_f32_e32 v104, v204, v104
	v_pk_mul_f32 v[110:111], v[110:111], v[114:115]
	v_exp_f32_e32 v114, v104
	v_sub_u32_e32 v104, 60, v184
	v_cvt_f32_ubyte0_e32 v104, v104
	v_mul_f32_e32 v104, v204, v104
	v_exp_f32_e32 v115, v104
	v_lshlrev_b32_e32 v104, 16, v105
	v_and_b32_e32 v105, 0xffff0000, v105
	s_waitcnt lgkmcnt(0)
	v_lshlrev_b32_e32 v116, 16, v106
	v_pk_mul_f32 v[114:115], v[114:115], v[104:105]
	v_xor_b32_e32 v104, 47, v184
	v_sub_u32_e32 v105, 46, v184
	v_cvt_f32_ubyte0_e32 v104, v104
	v_cvt_f32_ubyte0_e32 v105, v105
	v_mul_f32_e32 v104, v204, v104
	v_mul_f32_e32 v105, v204, v105
	v_exp_f32_e32 v104, v104
	v_exp_f32_e32 v105, v105
	v_and_b32_e32 v117, 0xffff0000, v106
	v_lshlrev_b32_e32 v106, 16, v107
	v_and_b32_e32 v107, 0xffff0000, v107
	v_pk_mul_f32 v[116:117], v[104:105], v[116:117]
	v_sub_u32_e32 v104, 45, v184
	v_sub_u32_e32 v105, 44, v184
	v_cvt_f32_ubyte0_e32 v104, v104
	v_cvt_f32_ubyte0_e32 v105, v105
	v_mul_f32_e32 v104, v204, v104
	v_mul_f32_e32 v105, v204, v105
	v_exp_f32_e32 v104, v104
	v_exp_f32_e32 v105, v105
	s_nop 0
	v_pk_mul_f32 v[118:119], v[104:105], v[106:107]
	v_cvt_pk_bf16_f32 v104, v110, v111
	v_add_u32_e32 v110, 0xfc00, v108
	v_cvt_pk_bf16_f32 v105, v114, v115
	ds_read_b64_tr_b16 v[108:109], v108 offset:64512
	ds_read_b64_tr_b16 v[110:111], v110 offset:4608
	v_exp_f32_e32 v114, v113
	v_sub_u32_e32 v113, 30, v184
	v_cvt_f32_ubyte0_e32 v113, v113
	v_mul_f32_e32 v113, v204, v113
	v_exp_f32_e32 v115, v113
	v_cvt_pk_bf16_f32 v106, v116, v117
	s_waitcnt lgkmcnt(1)
	v_lshlrev_b32_e32 v116, 16, v108
	v_and_b32_e32 v117, 0xffff0000, v108
	v_sub_u32_e32 v108, 29, v184
	v_cvt_f32_ubyte0_e32 v108, v108
	v_mul_f32_e32 v108, v204, v108
	v_pk_mul_f32 v[114:115], v[114:115], v[116:117]
	v_exp_f32_e32 v116, v108
	v_sub_u32_e32 v108, 28, v184
	v_cvt_f32_ubyte0_e32 v108, v108
	v_mul_f32_e32 v108, v204, v108
	v_exp_f32_e32 v117, v108
	v_lshlrev_b32_e32 v108, 16, v109
	v_and_b32_e32 v109, 0xffff0000, v109
	v_cvt_pk_bf16_f32 v107, v118, v119
	v_pk_mul_f32 v[116:117], v[116:117], v[108:109]
	v_xor_b32_e32 v108, 15, v184
	v_sub_u32_e32 v109, 14, v184
	v_cvt_f32_ubyte0_e32 v108, v108
	v_cvt_f32_ubyte0_e32 v109, v109
	v_mul_f32_e32 v108, v204, v108
	v_mul_f32_e32 v109, v204, v109
	v_exp_f32_e32 v108, v108
	v_exp_f32_e32 v109, v109
	s_waitcnt lgkmcnt(0)
; template <bool FWD> __device__ __forceinline__ void state_update_1(LAS unsigned char* lds, f32x4 (&racc)[8], float l2, int w, int g, unsigned qp, unsigned p) {
;     ...
; #pragma unroll
;     for (int nb = 0; nb < 8; ++nb) {
;         racc[nb] = racc[nb] * dec;
; #pragma unroll
;         for (int ks = 0; ks < 4; ++ks) racc[nb] = __builtin_amdgcn_mfma_f32_16x16x32_bf16(vs[ks], trfrag(lds + LK, 32 * ks + 4 * g, 32 * ks + 16 + 4 * g, nb, qp, p), racc[nb], 0, 0, 0);
;     }
	v_lshlrev_b32_e32 v118, 16, v110
	v_and_b32_e32 v119, 0xffff0000, v110
	v_lshlrev_b32_e32 v110, 16, v111
	v_pk_mul_f32 v[118:119], v[108:109], v[118:119]
	v_sub_u32_e32 v108, 13, v184
	v_sub_u32_e32 v109, 12, v184
	v_cvt_f32_ubyte0_e32 v108, v108
	v_cvt_f32_ubyte0_e32 v109, v109
	v_mul_f32_e32 v108, v204, v108
	v_mul_f32_e32 v109, v204, v109
	v_exp_f32_e32 v108, v108
	v_exp_f32_e32 v109, v109
	v_and_b32_e32 v111, 0xffff0000, v111
	v_pk_mul_f32 v[22:23], v[22:23], v[112:113] op_sel_hi:[1,0]
	v_pk_mul_f32 v[20:21], v[20:21], v[112:113] op_sel_hi:[1,0]
	v_pk_mul_f32 v[120:121], v[108:109], v[110:111]
	v_cvt_pk_bf16_f32 v108, v114, v115
	v_cvt_pk_bf16_f32 v109, v116, v117
	v_cvt_pk_bf16_f32 v110, v118, v119
	ds_read_b64_tr_b16 v[222:223], v205
	ds_read_b64_tr_b16 v[224:225], v205 offset:4608
	ds_read_b64_tr_b16 v[226:227], v205 offset:9216
	ds_read_b64_tr_b16 v[228:229], v205 offset:13824
	ds_read_b64_tr_b16 v[236:237], v205 offset:18432
	ds_read_b64_tr_b16 v[238:239], v205 offset:23040
	ds_read_b64_tr_b16 v[240:241], v205 offset:27648
	ds_read_b64_tr_b16 v[242:243], v205 offset:32256
	s_waitcnt lgkmcnt(6)
	v_mfma_f32_16x16x32_bf16 v[20:23], v[96:99], v[222:225], v[20:23]
	v_cvt_pk_bf16_f32 v111, v120, v121
	v_pk_mul_f32 v[2:3], v[2:3], v[112:113] op_sel_hi:[1,0]
	ds_read_b64_tr_b16 v[222:223], v205 offset:32
	ds_read_b64_tr_b16 v[224:225], v205 offset:4640
	s_waitcnt lgkmcnt(6)
	v_mfma_f32_16x16x32_bf16 v[20:23], v[100:103], v[226:229], v[20:23]
	v_pk_mul_f32 v[0:1], v[0:1], v[112:113] op_sel_hi:[1,0]
	v_pk_mul_f32 v[18:19], v[18:19], v[112:113] op_sel_hi:[1,0]
	ds_read_b64_tr_b16 v[226:227], v205 offset:9248
	ds_read_b64_tr_b16 v[228:229], v205 offset:13856
	s_waitcnt lgkmcnt(6)
	v_mfma_f32_16x16x32_bf16 v[20:23], v[104:107], v[236:239], v[20:23]
	v_pk_mul_f32 v[16:17], v[16:17], v[112:113] op_sel_hi:[1,0]
	ds_read_b64_tr_b16 v[236:237], v205 offset:18464
	ds_read_b64_tr_b16 v[238:239], v205 offset:23072
	s_waitcnt lgkmcnt(6)
	v_mfma_f32_16x16x32_bf16 v[20:23], v[108:111], v[240:243], v[20:23]
	v_pk_mul_f32 v[26:27], v[26:27], v[112:113] op_sel_hi:[1,0]
	v_pk_mul_f32 v[24:25], v[24:25], v[112:113] op_sel_hi:[1,0]
	ds_read_b64_tr_b16 v[240:241], v205 offset:27680
	ds_read_b64_tr_b16 v[242:243], v205 offset:32288
	s_waitcnt lgkmcnt(6)
	v_mfma_f32_16x16x32_bf16 v[0:3], v[96:99], v[222:225], v[0:3]
	v_mul_f32_e64 v6, v6, v112
	v_mul_f32_e64 v7, v7, v112
	v_pk_mul_f32 v[4:5], v[4:5], v[112:113] op_sel_hi:[1,0]
	v_pk_mul_f32 v[10:11], v[10:11], v[112:113] op_sel_hi:[1,0]
	ds_read_b64_tr_b16 v[222:223], v205 offset:64
	ds_read_b64_tr_b16 v[224:225], v205 offset:4672
	s_waitcnt lgkmcnt(6)
	v_mfma_f32_16x16x32_bf16 v[0:3], v[100:103], v[226:229], v[0:3]
	v_pk_mul_f32 v[8:9], v[8:9], v[112:113] op_sel_hi:[1,0]
	v_pk_mul_f32 v[14:15], v[14:15], v[112:113] op_sel_hi:[1,0]
	ds_read_b64_tr_b16 v[226:227], v205 offset:9280
	ds_read_b64_tr_b16 v[228:229], v205 offset:13888
	s_waitcnt lgkmcnt(6)
	v_mfma_f32_16x16x32_bf16 v[0:3], v[104:107], v[236:239], v[0:3]
	v_pk_mul_f32 v[12:13], v[12:13], v[112:113] op_sel_hi:[1,0]
	v_pk_mul_f32 v[30:31], v[30:31], v[112:113] op_sel_hi:[1,0]
	ds_read_b64_tr_b16 v[236:237], v205 offset:18496
	ds_read_b64_tr_b16 v[238:239], v205 offset:23104
	s_waitcnt lgkmcnt(6)
	v_mfma_f32_16x16x32_bf16 v[0:3], v[108:111], v[240:243], v[0:3]
	v_pk_mul_f32 v[28:29], v[28:29], v[112:113] op_sel_hi:[1,0]
	ds_read_b64_tr_b16 v[240:241], v205 offset:27712
	ds_read_b64_tr_b16 v[242:243], v205 offset:32320
	s_waitcnt lgkmcnt(6)
	v_mfma_f32_16x16x32_bf16 v[16:19], v[96:99], v[222:225], v[16:19]
	ds_read_b64_tr_b16 v[222:223], v205 offset:96
	ds_read_b64_tr_b16 v[224:225], v205 offset:4704
	s_waitcnt lgkmcnt(6)
	v_mfma_f32_16x16x32_bf16 v[16:19], v[100:103], v[226:229], v[16:19]
	ds_read_b64_tr_b16 v[226:227], v205 offset:9312
	ds_read_b64_tr_b16 v[228:229], v205 offset:13920
	s_waitcnt lgkmcnt(6)
; template <bool FWD> __device__ __forceinline__ void state_update_1(LAS unsigned char* lds, f32x4 (&racc)[8], float l2, int w, int g, unsigned qp, unsigned p) {
;     ...
; #pragma unroll
;     for (int nb = 0; nb < 8; ++nb) {
;         racc[nb] = racc[nb] * dec;
; #pragma unroll
;         for (int ks = 0; ks < 4; ++ks) racc[nb] = __builtin_amdgcn_mfma_f32_16x16x32_bf16(vs[ks], trfrag(lds + LK, 32 * ks + 4 * g, 32 * ks + 16 + 4 * g, nb, qp, p), racc[nb], 0, 0, 0);
;     }
	v_mfma_f32_16x16x32_bf16 v[16:19], v[104:107], v[236:239], v[16:19]
	ds_read_b64_tr_b16 v[236:237], v205 offset:18528
	ds_read_b64_tr_b16 v[238:239], v205 offset:23136
	s_waitcnt lgkmcnt(6)
	v_mfma_f32_16x16x32_bf16 v[16:19], v[108:111], v[240:243], v[16:19]
	ds_read_b64_tr_b16 v[240:241], v205 offset:27744
	ds_read_b64_tr_b16 v[242:243], v205 offset:32352
	s_waitcnt lgkmcnt(6)
	v_mfma_f32_16x16x32_bf16 v[24:27], v[96:99], v[222:225], v[24:27]
	ds_read_b64_tr_b16 v[222:223], v205 offset:128
	ds_read_b64_tr_b16 v[224:225], v205 offset:4736
	s_waitcnt lgkmcnt(6)
	v_mfma_f32_16x16x32_bf16 v[24:27], v[100:103], v[226:229], v[24:27]
	ds_read_b64_tr_b16 v[226:227], v205 offset:9344
	ds_read_b64_tr_b16 v[228:229], v205 offset:13952
	s_waitcnt lgkmcnt(6)
	v_mfma_f32_16x16x32_bf16 v[24:27], v[104:107], v[236:239], v[24:27]
	ds_read_b64_tr_b16 v[236:237], v205 offset:18560
	ds_read_b64_tr_b16 v[238:239], v205 offset:23168
	s_waitcnt lgkmcnt(6)
	v_mfma_f32_16x16x32_bf16 v[24:27], v[108:111], v[240:243], v[24:27]
	ds_read_b64_tr_b16 v[240:241], v205 offset:27776
	ds_read_b64_tr_b16 v[242:243], v205 offset:32384
	s_waitcnt lgkmcnt(6)
	v_mfma_f32_16x16x32_bf16 v[4:7], v[96:99], v[222:225], v[4:7]
	ds_read_b64_tr_b16 v[222:223], v205 offset:160
	ds_read_b64_tr_b16 v[224:225], v205 offset:4768
	s_waitcnt lgkmcnt(6)
	v_mfma_f32_16x16x32_bf16 v[4:7], v[100:103], v[226:229], v[4:7]
	ds_read_b64_tr_b16 v[226:227], v205 offset:9376
	ds_read_b64_tr_b16 v[228:229], v205 offset:13984
	s_waitcnt lgkmcnt(6)
	v_mfma_f32_16x16x32_bf16 v[4:7], v[104:107], v[236:239], v[4:7]
	ds_read_b64_tr_b16 v[236:237], v205 offset:18592
	ds_read_b64_tr_b16 v[238:239], v205 offset:23200
	s_waitcnt lgkmcnt(6)
	v_mfma_f32_16x16x32_bf16 v[4:7], v[108:111], v[240:243], v[4:7]
	ds_read_b64_tr_b16 v[240:241], v205 offset:27808
	ds_read_b64_tr_b16 v[242:243], v205 offset:32416
	s_waitcnt lgkmcnt(6)
	v_mfma_f32_16x16x32_bf16 v[8:11], v[96:99], v[222:225], v[8:11]
	ds_read_b64_tr_b16 v[222:223], v205 offset:192
	ds_read_b64_tr_b16 v[224:225], v205 offset:4800
	s_waitcnt lgkmcnt(6)
	v_mfma_f32_16x16x32_bf16 v[8:11], v[100:103], v[226:229], v[8:11]
	ds_read_b64_tr_b16 v[226:227], v205 offset:9408
	ds_read_b64_tr_b16 v[228:229], v205 offset:14016
	s_waitcnt lgkmcnt(6)
	v_mfma_f32_16x16x32_bf16 v[8:11], v[104:107], v[236:239], v[8:11]
	ds_read_b64_tr_b16 v[236:237], v205 offset:18624
	ds_read_b64_tr_b16 v[238:239], v205 offset:23232
	s_waitcnt lgkmcnt(6)
	v_mfma_f32_16x16x32_bf16 v[8:11], v[108:111], v[240:243], v[8:11]
	ds_read_b64_tr_b16 v[240:241], v205 offset:27840
	ds_read_b64_tr_b16 v[242:243], v205 offset:32448
	s_waitcnt lgkmcnt(6)
	v_mfma_f32_16x16x32_bf16 v[12:15], v[96:99], v[222:225], v[12:15]
	ds_read_b64_tr_b16 v[222:223], v205 offset:224
	ds_read_b64_tr_b16 v[224:225], v205 offset:4832
	s_waitcnt lgkmcnt(6)
	v_mfma_f32_16x16x32_bf16 v[12:15], v[100:103], v[226:229], v[12:15]
	ds_read_b64_tr_b16 v[226:227], v205 offset:9440
	ds_read_b64_tr_b16 v[228:229], v205 offset:14048
	s_waitcnt lgkmcnt(6)
	v_mfma_f32_16x16x32_bf16 v[12:15], v[104:107], v[236:239], v[12:15]
	ds_read_b64_tr_b16 v[236:237], v205 offset:18656
	ds_read_b64_tr_b16 v[238:239], v205 offset:23264
	s_waitcnt lgkmcnt(6)
	v_mfma_f32_16x16x32_bf16 v[12:15], v[108:111], v[240:243], v[12:15]
	ds_read_b64_tr_b16 v[240:241], v205 offset:27872
	ds_read_b64_tr_b16 v[242:243], v205 offset:32480
	s_waitcnt lgkmcnt(6)
	v_mfma_f32_16x16x32_bf16 v[28:31], v[96:99], v[222:225], v[28:31]
	s_waitcnt lgkmcnt(4)
	v_mfma_f32_16x16x32_bf16 v[28:31], v[100:103], v[226:229], v[28:31]
	s_waitcnt lgkmcnt(2)
	v_mfma_f32_16x16x32_bf16 v[28:31], v[104:107], v[236:239], v[28:31]
	s_waitcnt lgkmcnt(0)
	v_mfma_f32_16x16x32_bf16 v[28:31], v[108:111], v[240:243], v[28:31]
	s_cbranch_scc0 .LBB0_273
